# v63 + sigmoid denominators of the expert gate/up and layer-0 in-projection epilogues by v_rcp_f32 instead of the expanded IEEE division (f32 throughout)
# speedup vs baseline: 1.0232x; 1.0191x over previous
; __device__ __forceinline__ u32x4 pack8(const f32x4 v0, const f32x4 v1) { u32x4 w; w.x = cvt_pk_bf16(v0[0], v0[1]); w.y = cvt_pk_bf16(v0[2], v0[3]); w.z = cvt_pk_bf16(v1[0], v1[1]); w.w = cvt_pk_bf16(v1[2], v1[3]); return w; }
; __device__ __forceinline__ f32x4 sig4(const f32x4 v) { f32x4 r; r[0] = sigmoidf_(v[0]); r[1] = sigmoidf_(v[1]); r[2] = sigmoidf_(v[2]); r[3] = sigmoidf_(v[3]); return r; }
; __device__ __forceinline__ float sigmoidf_(float x) { return 1.0f / (1.0f + __expf(-x)); }
;     __device__ __forceinline__ void operator()(const f32x4 (&acc)[2][2][4][2], const pg8::Unit& u, int wr, int wc, int fr, int fq) const {
;     ...
;             if (u.pn < 2) {
; #pragma unroll
;                 for (int bj = 0; bj < 2; ++bj) *(u32x4*)(rp + u.pn * 256 + bj * 128 + cl) = pack8(acc[ai][bj][m][0], acc[ai][bj][m][1]);
;             } else {
;                 const f32x4 v0 = acc[ai][0][m][0] * sig4(acc[ai][1][m][0]), v1 = acc[ai][0][m][1] * sig4(acc[ai][1][m][1]);
;                 *(u32x4*)(rp + 512 + (u.pn - 2) * 128 + cl) = pack8(v0, v1);
;             } }
.LBB0_175:
	v_lshl_add_u32 v138, s30, 8, v144
	s_cmp_gt_i32 s6, 1
	s_cselect_b64 s[28:29], -1, 0
	s_lshl_b32 s7, s6, 7
	v_ashrrev_i32_e32 v139, 31, v138
	s_add_i32 s24, s7, 0xffffff00
	v_lshlrev_b64 v[140:141], 11, v[138:139]
	s_ashr_i32 s25, s24, 31
	v_lshl_add_u64 v[140:141], s[10:11], 0, v[140:141]
	s_mov_b64 s[30:31], -1
	s_and_b64 vcc, exec, s[28:29]
	v_lshlrev_b32_e32 v132, 1, v130
	s_cbranch_vccz .LBB0_177
	v_mul_f32_e32 v150, 0xbfb8aa3b, v118
	v_mul_f32_e32 v151, 0xbfb8aa3b, v119
	v_exp_f32_e32 v150, v150
	v_exp_f32_e32 v151, v151
	v_mul_f32_e32 v152, 0xbfb8aa3b, v120
	v_mul_f32_e32 v153, 0xbfb8aa3b, v121
	v_exp_f32_e32 v152, v152
	v_pk_add_f32 v[150:151], v[150:151], 1.0 op_sel_hi:[1,0]
	v_exp_f32_e32 v153, v153
	s_nop 0
	v_pk_add_f32 v[152:153], v[152:153], 1.0 op_sel_hi:[1,0]
	s_mov_b64 s[30:31], 0
	v_rcp_f32_e32 v151, v151
	v_rcp_f32_e32 v150, v150
	s_nop 0
	v_pk_mul_f32 v[150:151], v[126:127], v[150:151]
	v_rcp_f32_e32 v153, v153
	v_cvt_pk_bf16_f32 v150, v150, v151
	v_rcp_f32_e32 v152, v152
	v_mul_f32_e32 v154, 0xbfb8aa3b, v114
	v_mul_f32_e32 v155, 0xbfb8aa3b, v115
	v_exp_f32_e32 v154, v154
	v_exp_f32_e32 v155, v155
	v_mul_f32_e32 v156, 0xbfb8aa3b, v116
	v_mul_f32_e32 v157, 0xbfb8aa3b, v117
	v_exp_f32_e32 v156, v156
	v_pk_add_f32 v[154:155], v[154:155], 1.0 op_sel_hi:[1,0]
	v_exp_f32_e32 v157, v157
	s_nop 0
	v_pk_add_f32 v[156:157], v[156:157], 1.0 op_sel_hi:[1,0]
	v_pk_mul_f32 v[152:153], v[128:129], v[152:153]
	v_rcp_f32_e32 v155, v155
	v_cvt_pk_bf16_f32 v151, v152, v153
	v_rcp_f32_e32 v154, v154
	s_nop 0
	v_pk_mul_f32 v[154:155], v[122:123], v[154:155]
	v_rcp_f32_e32 v157, v157
	v_cvt_pk_bf16_f32 v152, v154, v155
	v_rcp_f32_e32 v156, v156
	s_nop 0
	v_pk_mul_f32 v[156:157], v[124:125], v[156:157]
	v_lshl_add_u64 v[154:155], s[24:25], 1, v[140:141]
	v_cvt_pk_bf16_f32 v153, v156, v157
	v_lshl_add_u64 v[154:155], v[154:155], 0, v[132:133]
	global_store_dwordx4 v[154:155], v[150:153], off offset:1024

; __device__ __forceinline__ u32x4 pack8(const f32x4 v0, const f32x4 v1) { u32x4 w; w.x = cvt_pk_bf16(v0[0], v0[1]); w.y = cvt_pk_bf16(v0[2], v0[3]); w.z = cvt_pk_bf16(v1[0], v1[1]); w.w = cvt_pk_bf16(v1[2], v1[3]); return w; }
; __device__ __forceinline__ f32x4 sig4(const f32x4 v) { f32x4 r; r[0] = sigmoidf_(v[0]); r[1] = sigmoidf_(v[1]); r[2] = sigmoidf_(v[2]); r[3] = sigmoidf_(v[3]); return r; }
; __device__ __forceinline__ float sigmoidf_(float x) { return 1.0f / (1.0f + __expf(-x)); }
;     __device__ __forceinline__ void operator()(const f32x4 (&acc)[2][2][4][2], const pg8::Unit& u, int wr, int wc, int fr, int fq) const {
;     ...
;             if (u.pn < 2) {
; #pragma unroll
;                 for (int bj = 0; bj < 2; ++bj) *(u32x4*)(rp + u.pn * 256 + bj * 128 + cl) = pack8(acc[ai][bj][m][0], acc[ai][bj][m][1]);
;             } else {
;                 const f32x4 v0 = acc[ai][0][m][0] * sig4(acc[ai][1][m][0]), v1 = acc[ai][0][m][1] * sig4(acc[ai][1][m][1]);
;                 *(u32x4*)(rp + 512 + (u.pn - 2) * 128 + cl) = pack8(v0, v1);
;             } }
.LBB0_179:
	v_or_b32_e32 v114, 16, v138
	v_ashrrev_i32_e32 v115, 31, v114
	v_lshlrev_b64 v[114:115], 11, v[114:115]
	v_cndmask_b32_e64 v116, 0, 1, s[28:29]
	v_lshl_add_u64 v[114:115], s[10:11], 0, v[114:115]
	v_cmp_ne_u32_e64 s[6:7], 1, v116
	s_andn2_b64 vcc, exec, s[28:29]
	s_mov_b64 s[28:29], -1
	s_cbranch_vccnz .LBB0_181
	v_mul_f32_e32 v116, 0xbfb8aa3b, v102
	v_mul_f32_e32 v117, 0xbfb8aa3b, v103
	v_exp_f32_e32 v116, v116
	v_exp_f32_e32 v117, v117
	v_mul_f32_e32 v118, 0xbfb8aa3b, v104
	v_mul_f32_e32 v119, 0xbfb8aa3b, v105
	v_exp_f32_e32 v118, v118
	v_pk_add_f32 v[116:117], v[116:117], 1.0 op_sel_hi:[1,0]
	v_exp_f32_e32 v119, v119
	s_nop 0
	v_pk_add_f32 v[118:119], v[118:119], 1.0 op_sel_hi:[1,0]
	v_rcp_f32_e32 v117, v117
	v_rcp_f32_e32 v116, v116
	s_nop 0
	v_pk_mul_f32 v[116:117], v[110:111], v[116:117]
	v_rcp_f32_e32 v119, v119
	v_cvt_pk_bf16_f32 v116, v116, v117
	v_rcp_f32_e32 v118, v118
	v_mul_f32_e32 v120, 0xbfb8aa3b, v98
	v_mul_f32_e32 v121, 0xbfb8aa3b, v99
	v_exp_f32_e32 v120, v120
	v_exp_f32_e32 v121, v121
	v_mul_f32_e32 v122, 0xbfb8aa3b, v100
	v_mul_f32_e32 v123, 0xbfb8aa3b, v101
	v_exp_f32_e32 v122, v122
	v_pk_add_f32 v[120:121], v[120:121], 1.0 op_sel_hi:[1,0]
	v_exp_f32_e32 v123, v123
	s_nop 0
	v_pk_add_f32 v[122:123], v[122:123], 1.0 op_sel_hi:[1,0]
	v_pk_mul_f32 v[118:119], v[112:113], v[118:119]
	v_rcp_f32_e32 v121, v121
	v_cvt_pk_bf16_f32 v117, v118, v119
	v_rcp_f32_e32 v120, v120
	s_nop 0
	v_pk_mul_f32 v[120:121], v[106:107], v[120:121]
	v_rcp_f32_e32 v123, v123
	v_cvt_pk_bf16_f32 v118, v120, v121
	v_rcp_f32_e32 v122, v122
	s_nop 0
	v_pk_mul_f32 v[122:123], v[108:109], v[122:123]
	v_lshl_add_u64 v[120:121], s[24:25], 1, v[114:115]
	v_cvt_pk_bf16_f32 v119, v122, v123
	v_lshl_add_u64 v[120:121], v[120:121], 0, v[132:133]
	s_mov_b64 s[28:29], 0
	global_store_dwordx4 v[120:121], v[116:119], off offset:1024

; __device__ __forceinline__ u32x4 pack8(const f32x4 v0, const f32x4 v1) { u32x4 w; w.x = cvt_pk_bf16(v0[0], v0[1]); w.y = cvt_pk_bf16(v0[2], v0[3]); w.z = cvt_pk_bf16(v1[0], v1[1]); w.w = cvt_pk_bf16(v1[2], v1[3]); return w; }
; __device__ __forceinline__ f32x4 sig4(const f32x4 v) { f32x4 r; r[0] = sigmoidf_(v[0]); r[1] = sigmoidf_(v[1]); r[2] = sigmoidf_(v[2]); r[3] = sigmoidf_(v[3]); return r; }
; __device__ __forceinline__ float sigmoidf_(float x) { return 1.0f / (1.0f + __expf(-x)); }
;     __device__ __forceinline__ void operator()(const f32x4 (&acc)[2][2][4][2], const pg8::Unit& u, int wr, int wc, int fr, int fq) const {
;     ...
;             if (u.pn < 2) {
; #pragma unroll
;                 for (int bj = 0; bj < 2; ++bj) *(u32x4*)(rp + u.pn * 256 + bj * 128 + cl) = pack8(acc[ai][bj][m][0], acc[ai][bj][m][1]);
;             } else {
;                 const f32x4 v0 = acc[ai][0][m][0] * sig4(acc[ai][1][m][0]), v1 = acc[ai][0][m][1] * sig4(acc[ai][1][m][1]);
;                 *(u32x4*)(rp + 512 + (u.pn - 2) * 128 + cl) = pack8(v0, v1);
;             } }
.LBB0_183:
	v_or_b32_e32 v98, 32, v138
	v_ashrrev_i32_e32 v99, 31, v98
	v_lshlrev_b64 v[98:99], 11, v[98:99]
	v_lshl_add_u64 v[98:99], s[10:11], 0, v[98:99]
	s_and_b64 vcc, exec, s[6:7]
	s_mov_b64 s[28:29], -1
	s_cbranch_vccnz .LBB0_185
	v_mul_f32_e32 v100, 0xbfb8aa3b, v86
	v_mul_f32_e32 v101, 0xbfb8aa3b, v87
	v_exp_f32_e32 v100, v100
	v_exp_f32_e32 v101, v101
	v_mul_f32_e32 v102, 0xbfb8aa3b, v88
	v_mul_f32_e32 v103, 0xbfb8aa3b, v89
	v_exp_f32_e32 v102, v102
	v_pk_add_f32 v[100:101], v[100:101], 1.0 op_sel_hi:[1,0]
	v_exp_f32_e32 v103, v103
	s_nop 0
	v_pk_add_f32 v[102:103], v[102:103], 1.0 op_sel_hi:[1,0]
	v_rcp_f32_e32 v101, v101
	v_rcp_f32_e32 v100, v100
	s_nop 0
	v_pk_mul_f32 v[100:101], v[94:95], v[100:101]
	v_rcp_f32_e32 v103, v103
	v_cvt_pk_bf16_f32 v100, v100, v101
	v_rcp_f32_e32 v102, v102
	v_mul_f32_e32 v104, 0xbfb8aa3b, v82
	v_mul_f32_e32 v105, 0xbfb8aa3b, v83
	v_exp_f32_e32 v104, v104
	v_exp_f32_e32 v105, v105
	v_mul_f32_e32 v106, 0xbfb8aa3b, v84
	v_mul_f32_e32 v107, 0xbfb8aa3b, v85
	v_exp_f32_e32 v106, v106
	v_pk_add_f32 v[104:105], v[104:105], 1.0 op_sel_hi:[1,0]
	v_exp_f32_e32 v107, v107
	s_nop 0
	v_pk_add_f32 v[106:107], v[106:107], 1.0 op_sel_hi:[1,0]
	v_pk_mul_f32 v[102:103], v[96:97], v[102:103]
	v_rcp_f32_e32 v105, v105
	v_cvt_pk_bf16_f32 v101, v102, v103
	v_rcp_f32_e32 v104, v104
	s_nop 0
	v_pk_mul_f32 v[104:105], v[90:91], v[104:105]
	v_rcp_f32_e32 v107, v107
	v_cvt_pk_bf16_f32 v102, v104, v105
	v_rcp_f32_e32 v106, v106
	s_nop 0
	v_pk_mul_f32 v[106:107], v[92:93], v[106:107]
	v_lshl_add_u64 v[104:105], s[24:25], 1, v[98:99]
	v_cvt_pk_bf16_f32 v103, v106, v107
	v_lshl_add_u64 v[104:105], v[104:105], 0, v[132:133]
	s_mov_b64 s[28:29], 0
	global_store_dwordx4 v[104:105], v[100:103], off offset:1024

; __device__ __forceinline__ u32x4 pack8(const f32x4 v0, const f32x4 v1) { u32x4 w; w.x = cvt_pk_bf16(v0[0], v0[1]); w.y = cvt_pk_bf16(v0[2], v0[3]); w.z = cvt_pk_bf16(v1[0], v1[1]); w.w = cvt_pk_bf16(v1[2], v1[3]); return w; }
; __device__ __forceinline__ f32x4 sig4(const f32x4 v) { f32x4 r; r[0] = sigmoidf_(v[0]); r[1] = sigmoidf_(v[1]); r[2] = sigmoidf_(v[2]); r[3] = sigmoidf_(v[3]); return r; }
; __device__ __forceinline__ float sigmoidf_(float x) { return 1.0f / (1.0f + __expf(-x)); }
;     __device__ __forceinline__ void operator()(const f32x4 (&acc)[2][2][4][2], const pg8::Unit& u, int wr, int wc, int fr, int fq) const {
;     ...
;             if (u.pn < 2) {
; #pragma unroll
;                 for (int bj = 0; bj < 2; ++bj) *(u32x4*)(rp + u.pn * 256 + bj * 128 + cl) = pack8(acc[ai][bj][m][0], acc[ai][bj][m][1]);
;             } else {
;                 const f32x4 v0 = acc[ai][0][m][0] * sig4(acc[ai][1][m][0]), v1 = acc[ai][0][m][1] * sig4(acc[ai][1][m][1]);
;                 *(u32x4*)(rp + 512 + (u.pn - 2) * 128 + cl) = pack8(v0, v1);
;             } }
.LBB0_187:
	v_or_b32_e32 v82, 48, v138
	v_ashrrev_i32_e32 v83, 31, v82
	v_lshlrev_b64 v[82:83], 11, v[82:83]
	v_lshl_add_u64 v[82:83], s[10:11], 0, v[82:83]
	s_and_b64 vcc, exec, s[6:7]
	s_mov_b64 s[28:29], -1
	s_cbranch_vccnz .LBB0_189
	v_mul_f32_e32 v84, 0xbfb8aa3b, v70
	v_mul_f32_e32 v85, 0xbfb8aa3b, v71
	v_exp_f32_e32 v84, v84
	v_exp_f32_e32 v85, v85
	v_mul_f32_e32 v86, 0xbfb8aa3b, v72
	v_mul_f32_e32 v87, 0xbfb8aa3b, v73
	v_exp_f32_e32 v86, v86
	v_pk_add_f32 v[84:85], v[84:85], 1.0 op_sel_hi:[1,0]
	v_exp_f32_e32 v87, v87
	s_nop 0
	v_pk_add_f32 v[86:87], v[86:87], 1.0 op_sel_hi:[1,0]
	v_rcp_f32_e32 v85, v85
	v_rcp_f32_e32 v84, v84
	s_nop 0
	v_pk_mul_f32 v[84:85], v[78:79], v[84:85]
	v_rcp_f32_e32 v87, v87
	v_cvt_pk_bf16_f32 v84, v84, v85
	v_rcp_f32_e32 v86, v86
	v_mul_f32_e32 v88, 0xbfb8aa3b, v66
	v_mul_f32_e32 v89, 0xbfb8aa3b, v67
	v_exp_f32_e32 v88, v88
	v_exp_f32_e32 v89, v89
	v_mul_f32_e32 v90, 0xbfb8aa3b, v68
	v_mul_f32_e32 v91, 0xbfb8aa3b, v69
	v_exp_f32_e32 v90, v90
	v_pk_add_f32 v[88:89], v[88:89], 1.0 op_sel_hi:[1,0]
	v_exp_f32_e32 v91, v91
	s_nop 0
	v_pk_add_f32 v[90:91], v[90:91], 1.0 op_sel_hi:[1,0]
	v_pk_mul_f32 v[86:87], v[80:81], v[86:87]
	v_rcp_f32_e32 v89, v89
	v_cvt_pk_bf16_f32 v85, v86, v87
	v_rcp_f32_e32 v88, v88
	s_nop 0
	v_pk_mul_f32 v[88:89], v[74:75], v[88:89]
	v_rcp_f32_e32 v91, v91
	v_cvt_pk_bf16_f32 v86, v88, v89
	v_rcp_f32_e32 v90, v90
	s_nop 0
	v_pk_mul_f32 v[90:91], v[76:77], v[90:91]
	v_lshl_add_u64 v[88:89], s[24:25], 1, v[82:83]
	v_cvt_pk_bf16_f32 v87, v90, v91
	v_lshl_add_u64 v[88:89], v[88:89], 0, v[132:133]
	s_mov_b64 s[28:29], 0
	global_store_dwordx4 v[88:89], v[84:87], off offset:1024

; __device__ __forceinline__ u32x4 pack8(const f32x4 v0, const f32x4 v1) { u32x4 w; w.x = cvt_pk_bf16(v0[0], v0[1]); w.y = cvt_pk_bf16(v0[2], v0[3]); w.z = cvt_pk_bf16(v1[0], v1[1]); w.w = cvt_pk_bf16(v1[2], v1[3]); return w; }
; __device__ __forceinline__ f32x4 sig4(const f32x4 v) { f32x4 r; r[0] = sigmoidf_(v[0]); r[1] = sigmoidf_(v[1]); r[2] = sigmoidf_(v[2]); r[3] = sigmoidf_(v[3]); return r; }
; __device__ __forceinline__ float sigmoidf_(float x) { return 1.0f / (1.0f + __expf(-x)); }
;     __device__ __forceinline__ void operator()(const f32x4 (&acc)[2][2][4][2], const pg8::Unit& u, int wr, int wc, int fr, int fq) const {
;     ...
;             if (u.pn < 2) {
; #pragma unroll
;                 for (int bj = 0; bj < 2; ++bj) *(u32x4*)(rp + u.pn * 256 + bj * 128 + cl) = pack8(acc[ai][bj][m][0], acc[ai][bj][m][1]);
;             } else {
;                 const f32x4 v0 = acc[ai][0][m][0] * sig4(acc[ai][1][m][0]), v1 = acc[ai][0][m][1] * sig4(acc[ai][1][m][1]);
;                 *(u32x4*)(rp + 512 + (u.pn - 2) * 128 + cl) = pack8(v0, v1);
;             } }
.LBB0_191:
	v_lshlrev_b64 v[66:67], 11, v[138:139]
	v_lshl_add_u64 v[66:67], s[10:11], 0, v[66:67]
	v_lshl_add_u64 v[66:67], v[66:67], 0, s[8:9]
	s_and_b64 vcc, exec, s[6:7]
	s_mov_b64 s[28:29], -1
	s_cbranch_vccnz .LBB0_193
	v_mul_f32_e32 v68, 0xbfb8aa3b, v54
	v_mul_f32_e32 v69, 0xbfb8aa3b, v55
	v_exp_f32_e32 v68, v68
	v_exp_f32_e32 v69, v69
	v_mul_f32_e32 v70, 0xbfb8aa3b, v56
	v_mul_f32_e32 v71, 0xbfb8aa3b, v57
	v_exp_f32_e32 v70, v70
	v_pk_add_f32 v[68:69], v[68:69], 1.0 op_sel_hi:[1,0]
	v_exp_f32_e32 v71, v71
	s_nop 0
	v_pk_add_f32 v[70:71], v[70:71], 1.0 op_sel_hi:[1,0]
	v_rcp_f32_e32 v69, v69
	v_rcp_f32_e32 v68, v68
	s_nop 0
	v_pk_mul_f32 v[68:69], v[62:63], v[68:69]
	v_rcp_f32_e32 v71, v71
	v_cvt_pk_bf16_f32 v68, v68, v69
	v_rcp_f32_e32 v70, v70
	v_mul_f32_e32 v72, 0xbfb8aa3b, v50
	v_mul_f32_e32 v73, 0xbfb8aa3b, v51
	v_exp_f32_e32 v72, v72
	v_exp_f32_e32 v73, v73
	v_mul_f32_e32 v74, 0xbfb8aa3b, v52
	v_mul_f32_e32 v75, 0xbfb8aa3b, v53
	v_exp_f32_e32 v74, v74
	v_pk_add_f32 v[72:73], v[72:73], 1.0 op_sel_hi:[1,0]
	v_exp_f32_e32 v75, v75
	s_nop 0
	v_pk_add_f32 v[74:75], v[74:75], 1.0 op_sel_hi:[1,0]
	v_pk_mul_f32 v[70:71], v[64:65], v[70:71]
	v_rcp_f32_e32 v73, v73
	v_cvt_pk_bf16_f32 v69, v70, v71
	v_rcp_f32_e32 v72, v72
	s_nop 0
	v_pk_mul_f32 v[72:73], v[58:59], v[72:73]
	v_rcp_f32_e32 v75, v75
	v_cvt_pk_bf16_f32 v70, v72, v73
	v_rcp_f32_e32 v74, v74
	s_nop 0
	v_pk_mul_f32 v[74:75], v[60:61], v[74:75]
	v_lshl_add_u64 v[72:73], s[24:25], 1, v[66:67]
	v_cvt_pk_bf16_f32 v71, v74, v75
	v_lshl_add_u64 v[72:73], v[72:73], 0, v[132:133]
	s_mov_b64 s[28:29], 0
	global_store_dwordx4 v[72:73], v[68:71], off offset:1024

; __device__ __forceinline__ u32x4 pack8(const f32x4 v0, const f32x4 v1) { u32x4 w; w.x = cvt_pk_bf16(v0[0], v0[1]); w.y = cvt_pk_bf16(v0[2], v0[3]); w.z = cvt_pk_bf16(v1[0], v1[1]); w.w = cvt_pk_bf16(v1[2], v1[3]); return w; }
; __device__ __forceinline__ f32x4 sig4(const f32x4 v) { f32x4 r; r[0] = sigmoidf_(v[0]); r[1] = sigmoidf_(v[1]); r[2] = sigmoidf_(v[2]); r[3] = sigmoidf_(v[3]); return r; }
; __device__ __forceinline__ float sigmoidf_(float x) { return 1.0f / (1.0f + __expf(-x)); }
;     __device__ __forceinline__ void operator()(const f32x4 (&acc)[2][2][4][2], const pg8::Unit& u, int wr, int wc, int fr, int fq) const {
;     ...
;             if (u.pn < 2) {
; #pragma unroll
;                 for (int bj = 0; bj < 2; ++bj) *(u32x4*)(rp + u.pn * 256 + bj * 128 + cl) = pack8(acc[ai][bj][m][0], acc[ai][bj][m][1]);
;             } else {
;                 const f32x4 v0 = acc[ai][0][m][0] * sig4(acc[ai][1][m][0]), v1 = acc[ai][0][m][1] * sig4(acc[ai][1][m][1]);
;                 *(u32x4*)(rp + 512 + (u.pn - 2) * 128 + cl) = pack8(v0, v1);
;             } }
.LBB0_195:
	v_lshlrev_b64 v[50:51], 11, v[138:139]
	v_lshl_add_u64 v[50:51], s[10:11], 0, v[50:51]
	v_lshl_add_u64 v[50:51], v[50:51], 0, s[14:15]
	s_and_b64 vcc, exec, s[6:7]
	s_mov_b64 s[28:29], -1
	s_cbranch_vccnz .LBB0_197
	v_mul_f32_e32 v52, 0xbfb8aa3b, v38
	v_mul_f32_e32 v53, 0xbfb8aa3b, v39
	v_exp_f32_e32 v52, v52
	v_exp_f32_e32 v53, v53
	v_mul_f32_e32 v54, 0xbfb8aa3b, v40
	v_mul_f32_e32 v55, 0xbfb8aa3b, v41
	v_exp_f32_e32 v54, v54
	v_pk_add_f32 v[52:53], v[52:53], 1.0 op_sel_hi:[1,0]
	v_exp_f32_e32 v55, v55
	s_nop 0
	v_pk_add_f32 v[54:55], v[54:55], 1.0 op_sel_hi:[1,0]
	v_rcp_f32_e32 v53, v53
	v_rcp_f32_e32 v52, v52
	s_nop 0
	v_pk_mul_f32 v[52:53], v[46:47], v[52:53]
	v_rcp_f32_e32 v55, v55
	v_cvt_pk_bf16_f32 v52, v52, v53
	v_rcp_f32_e32 v54, v54
	v_mul_f32_e32 v56, 0xbfb8aa3b, v34
	v_mul_f32_e32 v57, 0xbfb8aa3b, v35
	v_exp_f32_e32 v56, v56
	v_exp_f32_e32 v57, v57
	v_mul_f32_e32 v58, 0xbfb8aa3b, v36
	v_mul_f32_e32 v59, 0xbfb8aa3b, v37
	v_exp_f32_e32 v58, v58
	v_pk_add_f32 v[56:57], v[56:57], 1.0 op_sel_hi:[1,0]
	v_exp_f32_e32 v59, v59
	s_nop 0
	v_pk_add_f32 v[58:59], v[58:59], 1.0 op_sel_hi:[1,0]
	v_pk_mul_f32 v[54:55], v[48:49], v[54:55]
	v_rcp_f32_e32 v57, v57
	v_cvt_pk_bf16_f32 v53, v54, v55
	v_rcp_f32_e32 v56, v56
	s_nop 0
	v_pk_mul_f32 v[56:57], v[42:43], v[56:57]
	v_rcp_f32_e32 v59, v59
	v_cvt_pk_bf16_f32 v54, v56, v57
	v_rcp_f32_e32 v58, v58
	s_nop 0
	v_pk_mul_f32 v[58:59], v[44:45], v[58:59]
	v_lshl_add_u64 v[56:57], s[24:25], 1, v[50:51]
	v_cvt_pk_bf16_f32 v55, v58, v59
	v_lshl_add_u64 v[56:57], v[56:57], 0, v[132:133]
	s_mov_b64 s[28:29], 0
	global_store_dwordx4 v[56:57], v[52:55], off offset:1024

; __device__ __forceinline__ u32x4 pack8(const f32x4 v0, const f32x4 v1) { u32x4 w; w.x = cvt_pk_bf16(v0[0], v0[1]); w.y = cvt_pk_bf16(v0[2], v0[3]); w.z = cvt_pk_bf16(v1[0], v1[1]); w.w = cvt_pk_bf16(v1[2], v1[3]); return w; }
; __device__ __forceinline__ f32x4 sig4(const f32x4 v) { f32x4 r; r[0] = sigmoidf_(v[0]); r[1] = sigmoidf_(v[1]); r[2] = sigmoidf_(v[2]); r[3] = sigmoidf_(v[3]); return r; }
; __device__ __forceinline__ float sigmoidf_(float x) { return 1.0f / (1.0f + __expf(-x)); }
;     __device__ __forceinline__ void operator()(const f32x4 (&acc)[2][2][4][2], const pg8::Unit& u, int wr, int wc, int fr, int fq) const {
;     ...
;             if (u.pn < 2) {
; #pragma unroll
;                 for (int bj = 0; bj < 2; ++bj) *(u32x4*)(rp + u.pn * 256 + bj * 128 + cl) = pack8(acc[ai][bj][m][0], acc[ai][bj][m][1]);
;             } else {
;                 const f32x4 v0 = acc[ai][0][m][0] * sig4(acc[ai][1][m][0]), v1 = acc[ai][0][m][1] * sig4(acc[ai][1][m][1]);
;                 *(u32x4*)(rp + 512 + (u.pn - 2) * 128 + cl) = pack8(v0, v1);
;             } }
.LBB0_199:
	v_lshlrev_b64 v[34:35], 11, v[138:139]
	v_lshl_add_u64 v[34:35], s[10:11], 0, v[34:35]
	v_lshl_add_u64 v[34:35], v[34:35], 0, s[16:17]
	s_and_b64 vcc, exec, s[6:7]
	s_mov_b64 s[28:29], -1
	s_cbranch_vccnz .LBB0_201
	v_mul_f32_e32 v36, 0xbfb8aa3b, v22
	v_mul_f32_e32 v37, 0xbfb8aa3b, v23
	v_exp_f32_e32 v36, v36
	v_exp_f32_e32 v37, v37
	v_mul_f32_e32 v38, 0xbfb8aa3b, v24
	v_mul_f32_e32 v39, 0xbfb8aa3b, v25
	v_exp_f32_e32 v38, v38
	v_pk_add_f32 v[36:37], v[36:37], 1.0 op_sel_hi:[1,0]
	v_exp_f32_e32 v39, v39
	s_nop 0
	v_pk_add_f32 v[38:39], v[38:39], 1.0 op_sel_hi:[1,0]
	v_rcp_f32_e32 v37, v37
	v_rcp_f32_e32 v36, v36
	s_nop 0
	v_pk_mul_f32 v[36:37], v[30:31], v[36:37]
	v_rcp_f32_e32 v39, v39
	v_cvt_pk_bf16_f32 v36, v36, v37
	v_rcp_f32_e32 v38, v38
	v_mul_f32_e32 v40, 0xbfb8aa3b, v18
	v_mul_f32_e32 v41, 0xbfb8aa3b, v19
	v_exp_f32_e32 v40, v40
	v_exp_f32_e32 v41, v41
	v_mul_f32_e32 v42, 0xbfb8aa3b, v20
	v_mul_f32_e32 v43, 0xbfb8aa3b, v21
	v_exp_f32_e32 v42, v42
	v_pk_add_f32 v[40:41], v[40:41], 1.0 op_sel_hi:[1,0]
	v_exp_f32_e32 v43, v43
	s_nop 0
	v_pk_add_f32 v[42:43], v[42:43], 1.0 op_sel_hi:[1,0]
	v_pk_mul_f32 v[38:39], v[32:33], v[38:39]
	v_rcp_f32_e32 v41, v41
	v_cvt_pk_bf16_f32 v37, v38, v39
	v_rcp_f32_e32 v40, v40
	s_nop 0
	v_pk_mul_f32 v[40:41], v[26:27], v[40:41]
	v_rcp_f32_e32 v43, v43
	v_cvt_pk_bf16_f32 v38, v40, v41
	v_rcp_f32_e32 v42, v42
	s_nop 0
	v_pk_mul_f32 v[42:43], v[28:29], v[42:43]
	v_lshl_add_u64 v[40:41], s[24:25], 1, v[34:35]
	v_cvt_pk_bf16_f32 v39, v42, v43
	v_lshl_add_u64 v[40:41], v[40:41], 0, v[132:133]
	s_mov_b64 s[28:29], 0
	global_store_dwordx4 v[40:41], v[36:39], off offset:1024

; __device__ __forceinline__ u32x4 pack8(const f32x4 v0, const f32x4 v1) { u32x4 w; w.x = cvt_pk_bf16(v0[0], v0[1]); w.y = cvt_pk_bf16(v0[2], v0[3]); w.z = cvt_pk_bf16(v1[0], v1[1]); w.w = cvt_pk_bf16(v1[2], v1[3]); return w; }
; __device__ __forceinline__ f32x4 sig4(const f32x4 v) { f32x4 r; r[0] = sigmoidf_(v[0]); r[1] = sigmoidf_(v[1]); r[2] = sigmoidf_(v[2]); r[3] = sigmoidf_(v[3]); return r; }
; __device__ __forceinline__ float sigmoidf_(float x) { return 1.0f / (1.0f + __expf(-x)); }
;     __device__ __forceinline__ void operator()(const f32x4 (&acc)[2][2][4][2], const pg8::Unit& u, int wr, int wc, int fr, int fq) const {
;     ...
;             if (u.pn < 2) {
; #pragma unroll
;                 for (int bj = 0; bj < 2; ++bj) *(u32x4*)(rp + u.pn * 256 + bj * 128 + cl) = pack8(acc[ai][bj][m][0], acc[ai][bj][m][1]);
;             } else {
;                 const f32x4 v0 = acc[ai][0][m][0] * sig4(acc[ai][1][m][0]), v1 = acc[ai][0][m][1] * sig4(acc[ai][1][m][1]);
;                 *(u32x4*)(rp + 512 + (u.pn - 2) * 128 + cl) = pack8(v0, v1);
;             } }
.LBB0_203:
	v_lshlrev_b64 v[18:19], 11, v[138:139]
	v_lshl_add_u64 v[18:19], s[10:11], 0, v[18:19]
	v_lshl_add_u64 v[18:19], v[18:19], 0, s[18:19]
	s_and_b64 vcc, exec, s[6:7]
	s_mov_b64 s[6:7], -1
	s_cbranch_vccnz .LBB0_206
	v_mul_f32_e32 v20, 0xbfb8aa3b, v6
	v_mul_f32_e32 v21, 0xbfb8aa3b, v7
	v_exp_f32_e32 v20, v20
	v_exp_f32_e32 v21, v21
	v_mul_f32_e32 v22, 0xbfb8aa3b, v8
	v_mul_f32_e32 v23, 0xbfb8aa3b, v9
	v_exp_f32_e32 v22, v22
	v_pk_add_f32 v[20:21], v[20:21], 1.0 op_sel_hi:[1,0]
	v_exp_f32_e32 v23, v23
	s_nop 0
	v_pk_add_f32 v[22:23], v[22:23], 1.0 op_sel_hi:[1,0]
	v_rcp_f32_e32 v21, v21
	v_rcp_f32_e32 v20, v20
	s_nop 0
	v_pk_mul_f32 v[20:21], v[14:15], v[20:21]
	v_rcp_f32_e32 v23, v23
	v_cvt_pk_bf16_f32 v20, v20, v21
	v_rcp_f32_e32 v22, v22
	v_mul_f32_e32 v24, 0xbfb8aa3b, v2
	v_mul_f32_e32 v25, 0xbfb8aa3b, v3
	v_exp_f32_e32 v24, v24
	v_exp_f32_e32 v25, v25
	v_mul_f32_e32 v26, 0xbfb8aa3b, v4
	v_mul_f32_e32 v27, 0xbfb8aa3b, v5
	v_exp_f32_e32 v26, v26
	v_pk_add_f32 v[24:25], v[24:25], 1.0 op_sel_hi:[1,0]
	v_exp_f32_e32 v27, v27
	s_nop 0
	v_pk_add_f32 v[26:27], v[26:27], 1.0 op_sel_hi:[1,0]
	v_pk_mul_f32 v[22:23], v[16:17], v[22:23]
	v_rcp_f32_e32 v25, v25
	v_cvt_pk_bf16_f32 v21, v22, v23
	v_rcp_f32_e32 v24, v24
	s_nop 0
	v_pk_mul_f32 v[24:25], v[10:11], v[24:25]
	v_rcp_f32_e32 v27, v27
	v_cvt_pk_bf16_f32 v22, v24, v25
	v_rcp_f32_e32 v26, v26
	s_nop 0
	v_pk_mul_f32 v[26:27], v[12:13], v[26:27]
	v_lshl_add_u64 v[24:25], s[24:25], 1, v[18:19]
	v_cvt_pk_bf16_f32 v23, v26, v27
	v_lshl_add_u64 v[24:25], v[24:25], 0, v[132:133]
	global_store_dwordx4 v[24:25], v[20:23], off offset:1024
	s_cbranch_execz .LBB0_207

; __device__ __forceinline__ float clamp8(float v) { return __builtin_amdgcn_fmed3f(v, -448.0f, 448.0f); }
; __device__ __forceinline__ f32x4 sig4(const f32x4 v) { f32x4 r; r[0] = sigmoidf_(v[0]); r[1] = sigmoidf_(v[1]); r[2] = sigmoidf_(v[2]); r[3] = sigmoidf_(v[3]); return r; }
; #define EPI_ROWLOOP for (int ai = 0; ai < 2; ++ai) _Pragma("unroll") for (int m = 0; m < 4; ++m)
; __device__ __forceinline__ float sigmoidf_(float x) { return 1.0f / (1.0f + __expf(-x)); }
;     __device__ __forceinline__ void operator()(const f32x4 (&acc)[2][2][4][2], const pg8::Unit& u, int wr, int wc, int fr, int fq) const {
;         const int row0 = u.pm * 256 + wr * 64 + fr, c0 = (u.pn & 1) * 128 + wc * 32 + 8 * fq;
; #pragma unroll
;         EPI_ROWLOOP { const f32x4 g0 = acc[ai][0][m][0] * GU_SC, g1 = acc[ai][0][m][1] * GU_SC;
;             f32x4 h0 = g0 * sig4(g0) * (acc[ai][1][m][0] * (GU_SC * H8_SCALE)), h1 = g1 * sig4(g1) * (acc[ai][1][m][1] * (GU_SC * H8_SCALE));
; #pragma unroll
;             for (int i = 0; i < 4; ++i) { h0[i] = clamp8(h0[i]); h1[i] = clamp8(h1[i]); }
;             *(u32x2*)(HID + (size_t)(row0 + ai * 128 + m * 16) * 256 + c0) = pack8_fp8(h0, h1); }
;     }
.LBB0_760:
	v_pk_mul_f32 v[2:3], v[160:161], s[12:13] op_sel_hi:[1,0]
	v_pk_mul_f32 v[6:7], v[158:159], s[12:13] op_sel_hi:[1,0]
	v_mul_f32_e32 v8, 0xbfb8aa3b, v2
	v_mul_f32_e32 v9, 0xbfb8aa3b, v3
	v_exp_f32_e32 v8, v8
	v_exp_f32_e32 v9, v9
	v_mul_f32_e32 v5, 0xbfb8aa3b, v6
	v_exp_f32_e32 v10, v5
	v_mul_f32_e32 v5, 0xbfb8aa3b, v7
	v_pk_add_f32 v[8:9], v[8:9], 1.0 op_sel_hi:[1,0]
	v_exp_f32_e32 v11, v5
	s_nop 0
	v_pk_add_f32 v[10:11], v[10:11], 1.0 op_sel_hi:[1,0]
	v_pk_mul_f32 v[12:13], v[156:157], s[12:13] op_sel_hi:[1,0]
	v_pk_mul_f32 v[14:15], v[154:155], s[12:13] op_sel_hi:[1,0]
	v_rcp_f32_e32 v9, v9
	v_lshl_add_u32 v4, s54, 8, v168
	v_rcp_f32_e32 v8, v8
	s_nop 0
	v_pk_mul_f32 v[2:3], v[2:3], v[8:9]
	v_rcp_f32_e32 v11, v11
	v_pk_mul_f32 v[8:9], v[152:153], s[14:15] op_sel_hi:[1,0]
	v_mul_f32_e32 v16, 0xbfb8aa3b, v12
	v_mul_f32_e32 v17, 0xbfb8aa3b, v13
	v_exp_f32_e32 v16, v16
	v_exp_f32_e32 v17, v17
	v_rcp_f32_e32 v10, v10
	v_mul_f32_e32 v5, 0xbfb8aa3b, v14
	v_exp_f32_e32 v18, v5
	v_mul_f32_e32 v5, 0xbfb8aa3b, v15
	v_pk_add_f32 v[16:17], v[16:17], 1.0 op_sel_hi:[1,0]
	v_exp_f32_e32 v19, v5
	v_pk_mul_f32 v[6:7], v[6:7], v[10:11]
	v_pk_mul_f32 v[10:11], v[150:151], s[14:15] op_sel_hi:[1,0]
	v_pk_mul_f32 v[2:3], v[8:9], v[2:3]
	v_pk_mul_f32 v[6:7], v[10:11], v[6:7]
	v_pk_add_f32 v[8:9], v[18:19], 1.0 op_sel_hi:[1,0]
	v_rcp_f32_e32 v11, v17
	v_med3_f32 v7, v7, s50, v175
	v_rcp_f32_e32 v10, v16
	v_rcp_f32_e32 v9, v9
	v_rcp_f32_e32 v8, v8
	s_nop 0
	v_pk_mul_f32 v[8:9], v[14:15], v[8:9]
	v_pk_mul_f32 v[14:15], v[138:139], s[14:15] op_sel_hi:[1,0]
	v_med3_f32 v5, v6, s50, v175
	v_pk_mul_f32 v[8:9], v[14:15], v[8:9]
	v_mov_b32_e32 v6, v163
	v_med3_f32 v8, v8, s50, v175
	v_med3_f32 v9, v9, s50, v175
	v_cvt_pk_fp8_f32 v6, v5, v7
	v_mov_b32_e32 v7, v163
	v_cvt_pk_fp8_f32 v7, v8, v9
	v_pk_mul_f32 v[10:11], v[12:13], v[10:11]
	v_pk_mul_f32 v[12:13], v[140:141], s[14:15] op_sel_hi:[1,0]
	v_med3_f32 v2, v2, s50, v175
	v_pk_mul_f32 v[10:11], v[12:13], v[10:11]
	v_med3_f32 v3, v3, s50, v175
	v_med3_f32 v10, v10, s50, v175
	v_med3_f32 v5, v11, s50, v175
	s_lshl_b32 s17, s20, 7
	v_cvt_pk_fp8_f32 v6, v2, v3 op_sel:[0,0,1]
	v_cvt_pk_fp8_f32 v7, v10, v5 op_sel:[0,0,1]
	v_ashrrev_i32_e32 v5, 31, v4
	s_and_b32 s17, s17, 0x80
	v_lshlrev_b64 v[2:3], 8, v[4:5]
	v_or_b32_e32 v162, s17, v169
	v_lshl_add_u64 v[2:3], s[8:9], 0, v[2:3]
	v_lshl_add_u64 v[2:3], v[2:3], 0, v[162:163]
	global_store_dwordx2 v[2:3], v[6:7], off
	v_pk_mul_f32 v[6:7], v[148:149], s[12:13] op_sel_hi:[1,0]
	v_pk_mul_f32 v[8:9], v[146:147], s[12:13] op_sel_hi:[1,0]
	v_mul_f32_e32 v10, 0xbfb8aa3b, v6
	v_mul_f32_e32 v11, 0xbfb8aa3b, v7
	v_exp_f32_e32 v10, v10
	v_exp_f32_e32 v11, v11
	v_mul_f32_e32 v5, 0xbfb8aa3b, v8
	v_exp_f32_e32 v12, v5
	v_mul_f32_e32 v5, 0xbfb8aa3b, v9
	v_pk_add_f32 v[10:11], v[10:11], 1.0 op_sel_hi:[1,0]
	v_exp_f32_e32 v13, v5
	s_nop 0
	v_pk_add_f32 v[12:13], v[12:13], 1.0 op_sel_hi:[1,0]
	v_pk_mul_f32 v[14:15], v[144:145], s[12:13] op_sel_hi:[1,0]
	v_pk_mul_f32 v[16:17], v[142:143], s[12:13] op_sel_hi:[1,0]
	v_rcp_f32_e32 v11, v11
	v_rcp_f32_e32 v10, v10
	s_nop 0
	v_pk_mul_f32 v[6:7], v[6:7], v[10:11]
	v_rcp_f32_e32 v13, v13
	v_pk_mul_f32 v[10:11], v[136:137], s[14:15] op_sel_hi:[1,0]
	v_mul_f32_e32 v18, 0xbfb8aa3b, v14
	v_mul_f32_e32 v19, 0xbfb8aa3b, v15
	v_exp_f32_e32 v18, v18
	v_exp_f32_e32 v19, v19
	v_rcp_f32_e32 v12, v12
	v_mul_f32_e32 v5, 0xbfb8aa3b, v16
	v_exp_f32_e32 v20, v5
	v_mul_f32_e32 v5, 0xbfb8aa3b, v17
	v_pk_add_f32 v[18:19], v[18:19], 1.0 op_sel_hi:[1,0]
	v_exp_f32_e32 v21, v5
	v_pk_mul_f32 v[8:9], v[8:9], v[12:13]
	v_pk_mul_f32 v[12:13], v[134:135], s[14:15] op_sel_hi:[1,0]
	v_pk_mul_f32 v[6:7], v[10:11], v[6:7]
	v_pk_mul_f32 v[8:9], v[12:13], v[8:9]
	v_pk_add_f32 v[10:11], v[20:21], 1.0 op_sel_hi:[1,0]
	v_rcp_f32_e32 v13, v19
	v_med3_f32 v9, v9, s50, v175
	v_rcp_f32_e32 v12, v18
	v_rcp_f32_e32 v11, v11
	v_rcp_f32_e32 v10, v10
	s_nop 0
	v_pk_mul_f32 v[10:11], v[16:17], v[10:11]
	v_pk_mul_f32 v[16:17], v[130:131], s[14:15] op_sel_hi:[1,0]
	v_med3_f32 v5, v8, s50, v175
	v_pk_mul_f32 v[10:11], v[16:17], v[10:11]
	v_mov_b32_e32 v8, v163
	v_med3_f32 v10, v10, s50, v175
	v_med3_f32 v11, v11, s50, v175
	v_cvt_pk_fp8_f32 v8, v5, v9
	v_mov_b32_e32 v9, v163
	v_cvt_pk_fp8_f32 v9, v10, v11
	v_pk_mul_f32 v[12:13], v[14:15], v[12:13]
	v_pk_mul_f32 v[14:15], v[132:133], s[14:15] op_sel_hi:[1,0]
	v_med3_f32 v6, v6, s50, v175
	v_pk_mul_f32 v[12:13], v[14:15], v[12:13]
	v_med3_f32 v5, v7, s50, v175
	v_med3_f32 v12, v12, s50, v175
	v_med3_f32 v7, v13, s50, v175
	v_cvt_pk_fp8_f32 v8, v6, v5 op_sel:[0,0,1]
	v_or_b32_e32 v6, 16, v4
	v_cvt_pk_fp8_f32 v9, v12, v7 op_sel:[0,0,1]
	v_ashrrev_i32_e32 v7, 31, v6
	v_lshlrev_b64 v[6:7], 8, v[6:7]
	v_lshl_add_u64 v[6:7], s[8:9], 0, v[6:7]
	v_lshl_add_u64 v[6:7], v[6:7], 0, v[162:163]
	global_store_dwordx2 v[6:7], v[8:9], off
	v_pk_mul_f32 v[6:7], v[128:129], s[12:13] op_sel_hi:[1,0]
	v_pk_mul_f32 v[8:9], v[126:127], s[12:13] op_sel_hi:[1,0]
	v_mul_f32_e32 v10, 0xbfb8aa3b, v6
	v_mul_f32_e32 v11, 0xbfb8aa3b, v7
	v_exp_f32_e32 v10, v10
	v_exp_f32_e32 v11, v11
	v_mul_f32_e32 v5, 0xbfb8aa3b, v8
	v_exp_f32_e32 v12, v5
	v_mul_f32_e32 v5, 0xbfb8aa3b, v9
	v_pk_add_f32 v[10:11], v[10:11], 1.0 op_sel_hi:[1,0]
	v_exp_f32_e32 v13, v5
	s_nop 0
	v_pk_add_f32 v[12:13], v[12:13], 1.0 op_sel_hi:[1,0]
	v_pk_mul_f32 v[14:15], v[124:125], s[12:13] op_sel_hi:[1,0]
	v_pk_mul_f32 v[16:17], v[122:123], s[12:13] op_sel_hi:[1,0]
	v_rcp_f32_e32 v11, v11
	v_rcp_f32_e32 v10, v10
	s_nop 0
	v_pk_mul_f32 v[6:7], v[6:7], v[10:11]
	v_rcp_f32_e32 v13, v13
	v_pk_mul_f32 v[10:11], v[120:121], s[14:15] op_sel_hi:[1,0]
	v_mul_f32_e32 v18, 0xbfb8aa3b, v14
	v_mul_f32_e32 v19, 0xbfb8aa3b, v15
; __device__ __forceinline__ float clamp8(float v) { return __builtin_amdgcn_fmed3f(v, -448.0f, 448.0f); }
; __device__ __forceinline__ f32x4 sig4(const f32x4 v) { f32x4 r; r[0] = sigmoidf_(v[0]); r[1] = sigmoidf_(v[1]); r[2] = sigmoidf_(v[2]); r[3] = sigmoidf_(v[3]); return r; }
; #define EPI_ROWLOOP for (int ai = 0; ai < 2; ++ai) _Pragma("unroll") for (int m = 0; m < 4; ++m)
; __device__ __forceinline__ float sigmoidf_(float x) { return 1.0f / (1.0f + __expf(-x)); }
;     __device__ __forceinline__ void operator()(const f32x4 (&acc)[2][2][4][2], const pg8::Unit& u, int wr, int wc, int fr, int fq) const {
;         const int row0 = u.pm * 256 + wr * 64 + fr, c0 = (u.pn & 1) * 128 + wc * 32 + 8 * fq;
; #pragma unroll
;         EPI_ROWLOOP { const f32x4 g0 = acc[ai][0][m][0] * GU_SC, g1 = acc[ai][0][m][1] * GU_SC;
;             f32x4 h0 = g0 * sig4(g0) * (acc[ai][1][m][0] * (GU_SC * H8_SCALE)), h1 = g1 * sig4(g1) * (acc[ai][1][m][1] * (GU_SC * H8_SCALE));
; #pragma unroll
;             for (int i = 0; i < 4; ++i) { h0[i] = clamp8(h0[i]); h1[i] = clamp8(h1[i]); }
;             *(u32x2*)(HID + (size_t)(row0 + ai * 128 + m * 16) * 256 + c0) = pack8_fp8(h0, h1); }
	v_exp_f32_e32 v18, v18
	v_exp_f32_e32 v19, v19
	v_rcp_f32_e32 v12, v12
	v_mul_f32_e32 v5, 0xbfb8aa3b, v16
	v_exp_f32_e32 v20, v5
	v_mul_f32_e32 v5, 0xbfb8aa3b, v17
	v_pk_add_f32 v[18:19], v[18:19], 1.0 op_sel_hi:[1,0]
	v_exp_f32_e32 v21, v5
	v_pk_mul_f32 v[8:9], v[8:9], v[12:13]
	v_pk_mul_f32 v[12:13], v[118:119], s[14:15] op_sel_hi:[1,0]
	v_pk_mul_f32 v[6:7], v[10:11], v[6:7]
	v_pk_mul_f32 v[8:9], v[12:13], v[8:9]
	v_pk_add_f32 v[10:11], v[20:21], 1.0 op_sel_hi:[1,0]
	v_rcp_f32_e32 v13, v19
	v_med3_f32 v9, v9, s50, v175
	v_rcp_f32_e32 v12, v18
	v_rcp_f32_e32 v11, v11
	v_rcp_f32_e32 v10, v10
	s_nop 0
	v_pk_mul_f32 v[10:11], v[16:17], v[10:11]
	v_pk_mul_f32 v[16:17], v[106:107], s[14:15] op_sel_hi:[1,0]
	v_med3_f32 v5, v8, s50, v175
	v_pk_mul_f32 v[10:11], v[16:17], v[10:11]
	v_mov_b32_e32 v8, v163
	v_med3_f32 v10, v10, s50, v175
	v_med3_f32 v11, v11, s50, v175
	v_cvt_pk_fp8_f32 v8, v5, v9
	v_mov_b32_e32 v9, v163
	v_cvt_pk_fp8_f32 v9, v10, v11
	v_pk_mul_f32 v[12:13], v[14:15], v[12:13]
	v_pk_mul_f32 v[14:15], v[108:109], s[14:15] op_sel_hi:[1,0]
	v_med3_f32 v6, v6, s50, v175
	v_pk_mul_f32 v[12:13], v[14:15], v[12:13]
	v_med3_f32 v5, v7, s50, v175
	v_med3_f32 v12, v12, s50, v175
	v_med3_f32 v7, v13, s50, v175
	v_cvt_pk_fp8_f32 v8, v6, v5 op_sel:[0,0,1]
	v_or_b32_e32 v6, 32, v4
	v_cvt_pk_fp8_f32 v9, v12, v7 op_sel:[0,0,1]
	v_ashrrev_i32_e32 v7, 31, v6
	v_lshlrev_b64 v[6:7], 8, v[6:7]
	v_lshl_add_u64 v[6:7], s[8:9], 0, v[6:7]
	v_lshl_add_u64 v[6:7], v[6:7], 0, v[162:163]
	global_store_dwordx2 v[6:7], v[8:9], off
	v_pk_mul_f32 v[6:7], v[116:117], s[12:13] op_sel_hi:[1,0]
	v_pk_mul_f32 v[8:9], v[114:115], s[12:13] op_sel_hi:[1,0]
	v_mul_f32_e32 v10, 0xbfb8aa3b, v6
	v_mul_f32_e32 v11, 0xbfb8aa3b, v7
	v_exp_f32_e32 v10, v10
	v_exp_f32_e32 v11, v11
	v_mul_f32_e32 v5, 0xbfb8aa3b, v8
	v_exp_f32_e32 v12, v5
	v_mul_f32_e32 v5, 0xbfb8aa3b, v9
	v_pk_add_f32 v[10:11], v[10:11], 1.0 op_sel_hi:[1,0]
	v_exp_f32_e32 v13, v5
	s_nop 0
	v_pk_add_f32 v[12:13], v[12:13], 1.0 op_sel_hi:[1,0]
	v_pk_mul_f32 v[14:15], v[112:113], s[12:13] op_sel_hi:[1,0]
	v_pk_mul_f32 v[16:17], v[110:111], s[12:13] op_sel_hi:[1,0]
	v_rcp_f32_e32 v11, v11
	v_or_b32_e32 v4, 48, v4
	v_rcp_f32_e32 v10, v10
	s_nop 0
	v_pk_mul_f32 v[6:7], v[6:7], v[10:11]
	v_rcp_f32_e32 v13, v13
	v_pk_mul_f32 v[10:11], v[104:105], s[14:15] op_sel_hi:[1,0]
	v_mul_f32_e32 v18, 0xbfb8aa3b, v14
	v_mul_f32_e32 v19, 0xbfb8aa3b, v15
	v_exp_f32_e32 v18, v18
	v_exp_f32_e32 v19, v19
	v_rcp_f32_e32 v12, v12
	v_mul_f32_e32 v5, 0xbfb8aa3b, v16
	v_exp_f32_e32 v20, v5
	v_mul_f32_e32 v5, 0xbfb8aa3b, v17
	v_pk_add_f32 v[18:19], v[18:19], 1.0 op_sel_hi:[1,0]
	v_exp_f32_e32 v21, v5
	v_pk_mul_f32 v[8:9], v[8:9], v[12:13]
	v_pk_mul_f32 v[12:13], v[102:103], s[14:15] op_sel_hi:[1,0]
	v_pk_mul_f32 v[6:7], v[10:11], v[6:7]
	v_pk_mul_f32 v[8:9], v[12:13], v[8:9]
	v_pk_add_f32 v[10:11], v[20:21], 1.0 op_sel_hi:[1,0]
	v_rcp_f32_e32 v13, v19
	v_med3_f32 v9, v9, s50, v175
	v_rcp_f32_e32 v12, v18
	v_rcp_f32_e32 v11, v11
	v_rcp_f32_e32 v10, v10
	s_nop 0
	v_pk_mul_f32 v[10:11], v[16:17], v[10:11]
	v_pk_mul_f32 v[16:17], v[98:99], s[14:15] op_sel_hi:[1,0]
	v_med3_f32 v5, v8, s50, v175
	v_pk_mul_f32 v[10:11], v[16:17], v[10:11]
	v_mov_b32_e32 v8, v163
	v_med3_f32 v10, v10, s50, v175
	v_med3_f32 v11, v11, s50, v175
	v_cvt_pk_fp8_f32 v8, v5, v9
	v_mov_b32_e32 v9, v163
	v_cvt_pk_fp8_f32 v9, v10, v11
	v_pk_mul_f32 v[12:13], v[14:15], v[12:13]
	v_pk_mul_f32 v[14:15], v[100:101], s[14:15] op_sel_hi:[1,0]
	v_med3_f32 v6, v6, s50, v175
	v_pk_mul_f32 v[12:13], v[14:15], v[12:13]
	v_med3_f32 v5, v7, s50, v175
	v_med3_f32 v12, v12, s50, v175
	v_med3_f32 v7, v13, s50, v175
	v_cvt_pk_fp8_f32 v8, v6, v5 op_sel:[0,0,1]
	v_cvt_pk_fp8_f32 v9, v12, v7 op_sel:[0,0,1]
	v_ashrrev_i32_e32 v5, 31, v4
	v_lshlrev_b64 v[4:5], 8, v[4:5]
	v_lshl_add_u64 v[4:5], s[8:9], 0, v[4:5]
	v_lshl_add_u64 v[4:5], v[4:5], 0, v[162:163]
	global_store_dwordx2 v[4:5], v[8:9], off
	v_pk_mul_f32 v[4:5], v[96:97], s[12:13] op_sel_hi:[1,0]
	v_pk_mul_f32 v[6:7], v[94:95], s[12:13] op_sel_hi:[1,0]
	v_mul_f32_e32 v8, 0xbfb8aa3b, v4
	v_mul_f32_e32 v9, 0xbfb8aa3b, v5
	v_exp_f32_e32 v8, v8
	v_exp_f32_e32 v9, v9
	v_mul_f32_e32 v10, 0xbfb8aa3b, v6
	v_mul_f32_e32 v11, 0xbfb8aa3b, v7
	v_exp_f32_e32 v10, v10
	v_pk_add_f32 v[8:9], v[8:9], 1.0 op_sel_hi:[1,0]
	v_exp_f32_e32 v11, v11
	s_nop 0
	v_pk_add_f32 v[10:11], v[10:11], 1.0 op_sel_hi:[1,0]
	v_pk_mul_f32 v[12:13], v[92:93], s[12:13] op_sel_hi:[1,0]
	v_pk_mul_f32 v[14:15], v[90:91], s[12:13] op_sel_hi:[1,0]
	v_rcp_f32_e32 v9, v9
	v_rcp_f32_e32 v8, v8
	s_nop 0
	v_pk_mul_f32 v[4:5], v[4:5], v[8:9]
	v_rcp_f32_e32 v11, v11
	v_pk_mul_f32 v[8:9], v[88:89], s[14:15] op_sel_hi:[1,0]
	v_rcp_f32_e32 v10, v10
	v_mul_f32_e32 v16, 0xbfb8aa3b, v12
	v_mul_f32_e32 v17, 0xbfb8aa3b, v13
	v_exp_f32_e32 v16, v16
	v_exp_f32_e32 v17, v17
	v_mul_f32_e32 v18, 0xbfb8aa3b, v14
	v_mul_f32_e32 v19, 0xbfb8aa3b, v15
	v_pk_mul_f32 v[6:7], v[6:7], v[10:11]
	v_pk_add_f32 v[16:17], v[16:17], 1.0 op_sel_hi:[1,0]
	v_pk_mul_f32 v[10:11], v[86:87], s[14:15] op_sel_hi:[1,0]
	v_exp_f32_e32 v18, v18
	v_exp_f32_e32 v19, v19
	v_pk_mul_f32 v[6:7], v[10:11], v[6:7]
	v_pk_mul_f32 v[4:5], v[8:9], v[4:5]
	v_pk_add_f32 v[8:9], v[18:19], 1.0 op_sel_hi:[1,0]
	v_rcp_f32_e32 v11, v17
	v_rcp_f32_e32 v10, v16
	s_nop 0
	v_pk_mul_f32 v[10:11], v[12:13], v[10:11]
	v_rcp_f32_e32 v9, v9
	v_pk_mul_f32 v[12:13], v[76:77], s[14:15] op_sel_hi:[1,0]
	v_rcp_f32_e32 v8, v8
	s_nop 0
	v_pk_mul_f32 v[8:9], v[14:15], v[8:9]
	v_pk_mul_f32 v[14:15], v[74:75], s[14:15] op_sel_hi:[1,0]
	v_pk_mul_f32 v[10:11], v[12:13], v[10:11]
	v_pk_mul_f32 v[8:9], v[14:15], v[8:9]
	v_med3_f32 v12, v6, s50, v175
	v_med3_f32 v7, v7, s50, v175
; __device__ __forceinline__ float clamp8(float v) { return __builtin_amdgcn_fmed3f(v, -448.0f, 448.0f); }
; __device__ __forceinline__ f32x4 sig4(const f32x4 v) { f32x4 r; r[0] = sigmoidf_(v[0]); r[1] = sigmoidf_(v[1]); r[2] = sigmoidf_(v[2]); r[3] = sigmoidf_(v[3]); return r; }
; #define EPI_ROWLOOP for (int ai = 0; ai < 2; ++ai) _Pragma("unroll") for (int m = 0; m < 4; ++m)
; __device__ __forceinline__ float sigmoidf_(float x) { return 1.0f / (1.0f + __expf(-x)); }
;     __device__ __forceinline__ void operator()(const f32x4 (&acc)[2][2][4][2], const pg8::Unit& u, int wr, int wc, int fr, int fq) const {
;     ...
;         EPI_ROWLOOP { const f32x4 g0 = acc[ai][0][m][0] * GU_SC, g1 = acc[ai][0][m][1] * GU_SC;
;             f32x4 h0 = g0 * sig4(g0) * (acc[ai][1][m][0] * (GU_SC * H8_SCALE)), h1 = g1 * sig4(g1) * (acc[ai][1][m][1] * (GU_SC * H8_SCALE));
; #pragma unroll
;             for (int i = 0; i < 4; ++i) { h0[i] = clamp8(h0[i]); h1[i] = clamp8(h1[i]); }
;             *(u32x2*)(HID + (size_t)(row0 + ai * 128 + m * 16) * 256 + c0) = pack8_fp8(h0, h1); }
	v_mov_b32_e32 v6, v163
	v_med3_f32 v8, v8, s50, v175
	v_med3_f32 v9, v9, s50, v175
	v_cvt_pk_fp8_f32 v6, v12, v7
	v_mov_b32_e32 v7, v163
	v_cvt_pk_fp8_f32 v7, v8, v9
	v_med3_f32 v4, v4, s50, v175
	v_med3_f32 v5, v5, s50, v175
	v_med3_f32 v10, v10, s50, v175
	v_med3_f32 v8, v11, s50, v175
	v_cvt_pk_fp8_f32 v6, v4, v5 op_sel:[0,0,1]
	v_pk_mul_f32 v[4:5], v[84:85], s[12:13] op_sel_hi:[1,0]
	v_cvt_pk_fp8_f32 v7, v10, v8 op_sel:[0,0,1]
	v_mul_f32_e32 v10, 0xbfb8aa3b, v4
	v_mul_f32_e32 v11, 0xbfb8aa3b, v5
	v_exp_f32_e32 v10, v10
	v_exp_f32_e32 v11, v11
	v_pk_mul_f32 v[8:9], v[82:83], s[12:13] op_sel_hi:[1,0]
	v_pk_mul_f32 v[14:15], v[80:81], s[12:13] op_sel_hi:[1,0]
	v_mul_f32_e32 v12, 0xbfb8aa3b, v8
	v_pk_add_f32 v[10:11], v[10:11], 1.0 op_sel_hi:[1,0]
	v_mul_f32_e32 v13, 0xbfb8aa3b, v9
	v_exp_f32_e32 v12, v12
	v_exp_f32_e32 v13, v13
	v_pk_mul_f32 v[16:17], v[78:79], s[12:13] op_sel_hi:[1,0]
	v_rcp_f32_e32 v11, v11
	v_pk_add_f32 v[12:13], v[12:13], 1.0 op_sel_hi:[1,0]
	v_rcp_f32_e32 v10, v10
	s_nop 0
	v_pk_mul_f32 v[4:5], v[4:5], v[10:11]
	v_rcp_f32_e32 v13, v13
	v_pk_mul_f32 v[10:11], v[72:73], s[14:15] op_sel_hi:[1,0]
	v_rcp_f32_e32 v12, v12
	v_mul_f32_e32 v18, 0xbfb8aa3b, v14
	v_mul_f32_e32 v19, 0xbfb8aa3b, v15
	v_exp_f32_e32 v18, v18
	v_exp_f32_e32 v19, v19
	v_mul_f32_e32 v20, 0xbfb8aa3b, v16
	v_mul_f32_e32 v21, 0xbfb8aa3b, v17
	v_pk_mul_f32 v[8:9], v[8:9], v[12:13]
	v_pk_add_f32 v[18:19], v[18:19], 1.0 op_sel_hi:[1,0]
	v_pk_mul_f32 v[12:13], v[70:71], s[14:15] op_sel_hi:[1,0]
	v_exp_f32_e32 v20, v20
	v_exp_f32_e32 v21, v21
	v_pk_mul_f32 v[8:9], v[12:13], v[8:9]
	v_pk_mul_f32 v[4:5], v[10:11], v[4:5]
	v_pk_add_f32 v[10:11], v[20:21], 1.0 op_sel_hi:[1,0]
	v_rcp_f32_e32 v13, v19
	v_rcp_f32_e32 v12, v18
	s_nop 0
	v_pk_mul_f32 v[12:13], v[14:15], v[12:13]
	v_rcp_f32_e32 v11, v11
	v_pk_mul_f32 v[14:15], v[64:65], s[14:15] op_sel_hi:[1,0]
	v_rcp_f32_e32 v10, v10
	s_nop 0
	v_pk_mul_f32 v[10:11], v[16:17], v[10:11]
	v_pk_mul_f32 v[16:17], v[62:63], s[14:15] op_sel_hi:[1,0]
	v_pk_mul_f32 v[12:13], v[14:15], v[12:13]
	v_pk_mul_f32 v[10:11], v[16:17], v[10:11]
	v_med3_f32 v14, v8, s50, v175
	v_med3_f32 v9, v9, s50, v175
	v_mov_b32_e32 v8, v163
	v_med3_f32 v10, v10, s50, v175
	v_med3_f32 v11, v11, s50, v175
	v_cvt_pk_fp8_f32 v8, v14, v9
	v_mov_b32_e32 v9, v163
	v_cvt_pk_fp8_f32 v9, v10, v11
	v_med3_f32 v4, v4, s50, v175
	v_med3_f32 v12, v12, s50, v175
	v_med3_f32 v5, v5, s50, v175
	v_med3_f32 v10, v13, s50, v175
	v_cvt_pk_fp8_f32 v8, v4, v5 op_sel:[0,0,1]
	v_cvt_pk_fp8_f32 v9, v12, v10 op_sel:[0,0,1]
	v_add_co_u32_e32 v4, vcc, s51, v2
	v_pk_mul_f32 v[12:13], v[60:61], s[12:13] op_sel_hi:[1,0]
	s_nop 0
	v_addc_co_u32_e32 v5, vcc, 0, v3, vcc
	global_store_dwordx2 v[4:5], v[6:7], off offset:-4096
	global_store_dwordx2 v[4:5], v[8:9], off
	v_pk_mul_f32 v[4:5], v[68:69], s[12:13] op_sel_hi:[1,0]
	v_pk_mul_f32 v[6:7], v[66:67], s[12:13] op_sel_hi:[1,0]
	v_mul_f32_e32 v8, 0xbfb8aa3b, v4
	v_mul_f32_e32 v9, 0xbfb8aa3b, v5
	v_exp_f32_e32 v8, v8
	v_exp_f32_e32 v9, v9
	v_mul_f32_e32 v10, 0xbfb8aa3b, v6
	v_mul_f32_e32 v11, 0xbfb8aa3b, v7
	v_exp_f32_e32 v10, v10
	v_pk_add_f32 v[8:9], v[8:9], 1.0 op_sel_hi:[1,0]
	v_exp_f32_e32 v11, v11
	s_nop 0
	v_pk_add_f32 v[10:11], v[10:11], 1.0 op_sel_hi:[1,0]
	v_pk_mul_f32 v[14:15], v[58:59], s[12:13] op_sel_hi:[1,0]
	v_rcp_f32_e32 v9, v9
	v_rcp_f32_e32 v8, v8
	s_nop 0
	v_pk_mul_f32 v[4:5], v[4:5], v[8:9]
	v_rcp_f32_e32 v11, v11
	v_pk_mul_f32 v[8:9], v[56:57], s[14:15] op_sel_hi:[1,0]
	v_rcp_f32_e32 v10, v10
	v_mul_f32_e32 v16, 0xbfb8aa3b, v12
	v_mul_f32_e32 v17, 0xbfb8aa3b, v13
	v_exp_f32_e32 v16, v16
	v_exp_f32_e32 v17, v17
	v_mul_f32_e32 v18, 0xbfb8aa3b, v14
	v_mul_f32_e32 v19, 0xbfb8aa3b, v15
	v_pk_mul_f32 v[6:7], v[6:7], v[10:11]
; __device__ __forceinline__ float clamp8(float v) { return __builtin_amdgcn_fmed3f(v, -448.0f, 448.0f); }
; #define PG8_BAR __builtin_amdgcn_s_barrier()
; #define PG8_ZERO_W() do { if constexpr (F8) { _Pragma("unroll") for (int _a = 0; _a < 2; ++_a) _Pragma("unroll") for (int _b = 0; _b < 2; ++_b) _Pragma("unroll") for (int _m = 0; _m < 2; ++_m) _Pragma("unroll") for (int _e = 0; _e < 16; ++_e) accw[_a][_b][_m][_e] = 0.f; } } while (0)
; __device__ __forceinline__ f32x4 sig4(const f32x4 v) { f32x4 r; r[0] = sigmoidf_(v[0]); r[1] = sigmoidf_(v[1]); r[2] = sigmoidf_(v[2]); r[3] = sigmoidf_(v[3]); return r; }
; #define EPI_ROWLOOP for (int ai = 0; ai < 2; ++ai) _Pragma("unroll") for (int m = 0; m < 4; ++m)
;     ...
;         E(acc, cur, wr, wc, fr, fq);
;         PG8_ZERO_W();
;         if (!has_next) break;
; #pragma unroll
;         for (int a = 0; a < 2; ++a)
; #pragma unroll
;             for (int b = 0; b < 2; ++b)
; #pragma unroll
;                 for (int m = 0; m < 4; ++m)
; #pragma unroll
;                     for (int n = 0; n < 2; ++n) acc[a][b][m][n] = (f32x4){0.f, 0.f, 0.f, 0.f};
;         cur = nxt; cB = nB; ++ui;
; #pragma unroll
;         for (int h = 0; h < 2; ++h) { uC[h] = uN[h];
; #pragma unroll
;             for (int i = 0; i < 2; ++i) aoC[h][i] = aoN[h][i]; }
;         if constexpr (ALIGN_EPI) { if (wr == 1) PG8_BAR; }
;     __device__ __forceinline__ void operator()(const f32x4 (&acc)[2][2][4][2], const pg8::Unit& u, int wr, int wc, int fr, int fq) const {
;     ...
;         EPI_ROWLOOP { const f32x4 g0 = acc[ai][0][m][0] * GU_SC, g1 = acc[ai][0][m][1] * GU_SC;
;             f32x4 h0 = g0 * sig4(g0) * (acc[ai][1][m][0] * (GU_SC * H8_SCALE)), h1 = g1 * sig4(g1) * (acc[ai][1][m][1] * (GU_SC * H8_SCALE));
; #pragma unroll
;             for (int i = 0; i < 4; ++i) { h0[i] = clamp8(h0[i]); h1[i] = clamp8(h1[i]); }
;             *(u32x2*)(HID + (size_t)(row0 + ai * 128 + m * 16) * 256 + c0) = pack8_fp8(h0, h1); }
	v_pk_add_f32 v[16:17], v[16:17], 1.0 op_sel_hi:[1,0]
	v_pk_mul_f32 v[10:11], v[54:55], s[14:15] op_sel_hi:[1,0]
	v_exp_f32_e32 v18, v18
	v_exp_f32_e32 v19, v19
	v_pk_mul_f32 v[6:7], v[10:11], v[6:7]
	v_pk_mul_f32 v[4:5], v[8:9], v[4:5]
	v_pk_add_f32 v[8:9], v[18:19], 1.0 op_sel_hi:[1,0]
	v_rcp_f32_e32 v11, v17
	v_rcp_f32_e32 v10, v16
	s_nop 0
	v_pk_mul_f32 v[10:11], v[12:13], v[10:11]
	v_rcp_f32_e32 v9, v9
	v_pk_mul_f32 v[12:13], v[44:45], s[14:15] op_sel_hi:[1,0]
	v_rcp_f32_e32 v8, v8
	s_nop 0
	v_pk_mul_f32 v[8:9], v[14:15], v[8:9]
	v_pk_mul_f32 v[14:15], v[42:43], s[14:15] op_sel_hi:[1,0]
	v_pk_mul_f32 v[10:11], v[12:13], v[10:11]
	v_pk_mul_f32 v[8:9], v[14:15], v[8:9]
	v_med3_f32 v12, v6, s50, v175
	v_med3_f32 v7, v7, s50, v175
	v_mov_b32_e32 v6, v163
	v_med3_f32 v8, v8, s50, v175
	v_med3_f32 v9, v9, s50, v175
	v_cvt_pk_fp8_f32 v6, v12, v7
	v_mov_b32_e32 v7, v163
	v_cvt_pk_fp8_f32 v7, v8, v9
	v_med3_f32 v4, v4, s50, v175
	v_med3_f32 v10, v10, s50, v175
	v_med3_f32 v5, v5, s50, v175
	v_med3_f32 v8, v11, s50, v175
	v_cvt_pk_fp8_f32 v6, v4, v5 op_sel:[0,0,1]
	v_cvt_pk_fp8_f32 v7, v10, v8 op_sel:[0,0,1]
	v_add_co_u32_e32 v4, vcc, s47, v2
	v_pk_mul_f32 v[12:13], v[48:49], s[12:13] op_sel_hi:[1,0]
	s_nop 0
	v_addc_co_u32_e32 v5, vcc, 0, v3, vcc
	global_store_dwordx2 v[4:5], v[6:7], off
	v_pk_mul_f32 v[4:5], v[52:53], s[12:13] op_sel_hi:[1,0]
	v_pk_mul_f32 v[6:7], v[50:51], s[12:13] op_sel_hi:[1,0]
	v_mul_f32_e32 v8, 0xbfb8aa3b, v4
	v_mul_f32_e32 v9, 0xbfb8aa3b, v5
	v_exp_f32_e32 v8, v8
	v_exp_f32_e32 v9, v9
	v_mul_f32_e32 v10, 0xbfb8aa3b, v6
	v_mul_f32_e32 v11, 0xbfb8aa3b, v7
	v_exp_f32_e32 v10, v10
	v_pk_add_f32 v[8:9], v[8:9], 1.0 op_sel_hi:[1,0]
	v_exp_f32_e32 v11, v11
	s_nop 0
	v_pk_add_f32 v[10:11], v[10:11], 1.0 op_sel_hi:[1,0]
	v_pk_mul_f32 v[14:15], v[46:47], s[12:13] op_sel_hi:[1,0]
	v_rcp_f32_e32 v9, v9
	v_rcp_f32_e32 v8, v8
	s_nop 0
	v_pk_mul_f32 v[4:5], v[4:5], v[8:9]
	v_rcp_f32_e32 v11, v11
	v_pk_mul_f32 v[8:9], v[40:41], s[14:15] op_sel_hi:[1,0]
	v_rcp_f32_e32 v10, v10
	v_mul_f32_e32 v16, 0xbfb8aa3b, v12
	v_mul_f32_e32 v17, 0xbfb8aa3b, v13
	v_exp_f32_e32 v16, v16
	v_exp_f32_e32 v17, v17
	v_mul_f32_e32 v18, 0xbfb8aa3b, v14
	v_mul_f32_e32 v19, 0xbfb8aa3b, v15
	v_pk_mul_f32 v[6:7], v[6:7], v[10:11]
	v_pk_add_f32 v[16:17], v[16:17], 1.0 op_sel_hi:[1,0]
	v_pk_mul_f32 v[10:11], v[38:39], s[14:15] op_sel_hi:[1,0]
	v_exp_f32_e32 v18, v18
	v_exp_f32_e32 v19, v19
	v_pk_mul_f32 v[6:7], v[10:11], v[6:7]
	v_pk_mul_f32 v[4:5], v[8:9], v[4:5]
	v_pk_add_f32 v[8:9], v[18:19], 1.0 op_sel_hi:[1,0]
	v_rcp_f32_e32 v11, v17
	v_rcp_f32_e32 v10, v16
	s_nop 0
	v_pk_mul_f32 v[10:11], v[12:13], v[10:11]
	v_rcp_f32_e32 v9, v9
	v_pk_mul_f32 v[12:13], v[36:37], s[14:15] op_sel_hi:[1,0]
	v_rcp_f32_e32 v8, v8
	s_nop 0
	v_pk_mul_f32 v[8:9], v[14:15], v[8:9]
	v_pk_mul_f32 v[14:15], v[34:35], s[14:15] op_sel_hi:[1,0]
	v_pk_mul_f32 v[10:11], v[12:13], v[10:11]
	v_pk_mul_f32 v[8:9], v[14:15], v[8:9]
	v_med3_f32 v12, v6, s50, v175
	v_med3_f32 v7, v7, s50, v175
	v_mov_b32_e32 v6, v163
	v_med3_f32 v8, v8, s50, v175
	v_med3_f32 v9, v9, s50, v175
	v_cvt_pk_fp8_f32 v6, v12, v7
	v_mov_b32_e32 v7, v163
	v_cvt_pk_fp8_f32 v7, v8, v9
	v_med3_f32 v4, v4, s50, v175
	v_med3_f32 v10, v10, s50, v175
	v_med3_f32 v5, v5, s50, v175
	v_med3_f32 v8, v11, s50, v175
	v_cvt_pk_fp8_f32 v6, v4, v5 op_sel:[0,0,1]
	v_cvt_pk_fp8_f32 v7, v10, v8 op_sel:[0,0,1]
	v_add_co_u32_e32 v2, vcc, 0xb000, v2
	s_nop 1
	v_addc_co_u32_e32 v3, vcc, 0, v3, vcc
	global_store_dwordx2 v[2:3], v[6:7], off
	s_load_dwordx2 s[58:59], s[82:83], 0x118
	s_and_b64 vcc, exec, s[4:5]
	s_mov_b64 s[4:5], -1
	s_cbranch_vccnz .LBB0_743
	s_andn2_b64 vcc, exec, s[6:7]
	s_cbranch_vccnz .LBB0_742
	s_barrier
	s_branch .LBB0_742

; __device__ __forceinline__ float clamp8(float v) { return __builtin_amdgcn_fmed3f(v, -448.0f, 448.0f); }
; __device__ __forceinline__ f32x4 sig4(const f32x4 v) { f32x4 r; r[0] = sigmoidf_(v[0]); r[1] = sigmoidf_(v[1]); r[2] = sigmoidf_(v[2]); r[3] = sigmoidf_(v[3]); return r; }
; #define EPI_ROWLOOP for (int ai = 0; ai < 2; ++ai) _Pragma("unroll") for (int m = 0; m < 4; ++m)
; __device__ __forceinline__ float sigmoidf_(float x) { return 1.0f / (1.0f + __expf(-x)); }
;     __device__ __forceinline__ void operator()(const f32x4 (&acc)[2][2][4][2], const pg8::Unit& u, int wr, int wc, int fr, int fq) const {
;         const int row0 = u.pm * 256 + wr * 64 + fr, c0 = (u.pn & 1) * 128 + wc * 32 + 8 * fq;
; #pragma unroll
;         EPI_ROWLOOP { const f32x4 g0 = acc[ai][0][m][0] * GU_SC, g1 = acc[ai][0][m][1] * GU_SC;
;             f32x4 h0 = g0 * sig4(g0) * (acc[ai][1][m][0] * (GU_SC * H8_SCALE)), h1 = g1 * sig4(g1) * (acc[ai][1][m][1] * (GU_SC * H8_SCALE));
; #pragma unroll
;             for (int i = 0; i < 4; ++i) { h0[i] = clamp8(h0[i]); h1[i] = clamp8(h1[i]); }
;             *(u32x2*)(HID + (size_t)(row0 + ai * 128 + m * 16) * 256 + c0) = pack8_fp8(h0, h1); }
.LBB0_2711:
	v_pk_mul_f32 v[2:3], v[160:161], s[12:13] op_sel_hi:[1,0]
	v_pk_mul_f32 v[6:7], v[158:159], s[12:13] op_sel_hi:[1,0]
	v_mul_f32_e32 v8, 0xbfb8aa3b, v2
	v_mul_f32_e32 v9, 0xbfb8aa3b, v3
	v_exp_f32_e32 v8, v8
	v_exp_f32_e32 v9, v9
	v_mul_f32_e32 v5, 0xbfb8aa3b, v6
	v_exp_f32_e32 v10, v5
	v_mul_f32_e32 v5, 0xbfb8aa3b, v7
	v_pk_add_f32 v[8:9], v[8:9], 1.0 op_sel_hi:[1,0]
	v_exp_f32_e32 v11, v5
	s_nop 0
	v_pk_add_f32 v[10:11], v[10:11], 1.0 op_sel_hi:[1,0]
	v_pk_mul_f32 v[12:13], v[156:157], s[12:13] op_sel_hi:[1,0]
	v_pk_mul_f32 v[14:15], v[154:155], s[12:13] op_sel_hi:[1,0]
	v_rcp_f32_e32 v9, v9
	v_lshl_add_u32 v4, s54, 8, v168
	v_rcp_f32_e32 v8, v8
	s_nop 0
	v_pk_mul_f32 v[2:3], v[2:3], v[8:9]
	v_rcp_f32_e32 v11, v11
	v_pk_mul_f32 v[8:9], v[152:153], s[14:15] op_sel_hi:[1,0]
	v_mul_f32_e32 v16, 0xbfb8aa3b, v12
	v_mul_f32_e32 v17, 0xbfb8aa3b, v13
	v_exp_f32_e32 v16, v16
	v_exp_f32_e32 v17, v17
	v_rcp_f32_e32 v10, v10
	v_mul_f32_e32 v5, 0xbfb8aa3b, v14
	v_exp_f32_e32 v18, v5
	v_mul_f32_e32 v5, 0xbfb8aa3b, v15
	v_pk_add_f32 v[16:17], v[16:17], 1.0 op_sel_hi:[1,0]
	v_exp_f32_e32 v19, v5
	v_pk_mul_f32 v[6:7], v[6:7], v[10:11]
	v_pk_mul_f32 v[10:11], v[150:151], s[14:15] op_sel_hi:[1,0]
	v_pk_mul_f32 v[2:3], v[8:9], v[2:3]
	v_pk_mul_f32 v[6:7], v[10:11], v[6:7]
	v_pk_add_f32 v[8:9], v[18:19], 1.0 op_sel_hi:[1,0]
	v_rcp_f32_e32 v11, v17
	v_med3_f32 v7, v7, s50, v175
	v_rcp_f32_e32 v10, v16
	v_rcp_f32_e32 v9, v9
	v_rcp_f32_e32 v8, v8
	s_nop 0
	v_pk_mul_f32 v[8:9], v[14:15], v[8:9]
	v_pk_mul_f32 v[14:15], v[138:139], s[14:15] op_sel_hi:[1,0]
	v_med3_f32 v5, v6, s50, v175
	v_pk_mul_f32 v[8:9], v[14:15], v[8:9]
	v_mov_b32_e32 v6, v163
	v_med3_f32 v8, v8, s50, v175
	v_med3_f32 v9, v9, s50, v175
	v_cvt_pk_fp8_f32 v6, v5, v7
	v_mov_b32_e32 v7, v163
	v_cvt_pk_fp8_f32 v7, v8, v9
	v_pk_mul_f32 v[10:11], v[12:13], v[10:11]
	v_pk_mul_f32 v[12:13], v[140:141], s[14:15] op_sel_hi:[1,0]
	v_med3_f32 v2, v2, s50, v175
	v_pk_mul_f32 v[10:11], v[12:13], v[10:11]
	v_med3_f32 v3, v3, s50, v175
	v_med3_f32 v10, v10, s50, v175
	v_med3_f32 v5, v11, s50, v175
	s_lshl_b32 s17, s20, 7
	v_cvt_pk_fp8_f32 v6, v2, v3 op_sel:[0,0,1]
	v_cvt_pk_fp8_f32 v7, v10, v5 op_sel:[0,0,1]
	v_ashrrev_i32_e32 v5, 31, v4
	s_and_b32 s17, s17, 0x80
	v_lshlrev_b64 v[2:3], 8, v[4:5]
	v_or_b32_e32 v162, s17, v169
	v_lshl_add_u64 v[2:3], s[8:9], 0, v[2:3]
	v_lshl_add_u64 v[2:3], v[2:3], 0, v[162:163]
	global_store_dwordx2 v[2:3], v[6:7], off
	v_pk_mul_f32 v[6:7], v[148:149], s[12:13] op_sel_hi:[1,0]
	v_pk_mul_f32 v[8:9], v[146:147], s[12:13] op_sel_hi:[1,0]
	v_mul_f32_e32 v10, 0xbfb8aa3b, v6
	v_mul_f32_e32 v11, 0xbfb8aa3b, v7
	v_exp_f32_e32 v10, v10
	v_exp_f32_e32 v11, v11
	v_mul_f32_e32 v5, 0xbfb8aa3b, v8
	v_exp_f32_e32 v12, v5
	v_mul_f32_e32 v5, 0xbfb8aa3b, v9
	v_pk_add_f32 v[10:11], v[10:11], 1.0 op_sel_hi:[1,0]
	v_exp_f32_e32 v13, v5
	s_nop 0
	v_pk_add_f32 v[12:13], v[12:13], 1.0 op_sel_hi:[1,0]
	v_pk_mul_f32 v[14:15], v[144:145], s[12:13] op_sel_hi:[1,0]
	v_pk_mul_f32 v[16:17], v[142:143], s[12:13] op_sel_hi:[1,0]
	v_rcp_f32_e32 v11, v11
	v_readlane_b32 s58, v252, 4
	v_rcp_f32_e32 v10, v10
	s_nop 0
	v_pk_mul_f32 v[6:7], v[6:7], v[10:11]
	v_rcp_f32_e32 v13, v13
	v_pk_mul_f32 v[10:11], v[136:137], s[14:15] op_sel_hi:[1,0]
	v_mul_f32_e32 v18, 0xbfb8aa3b, v14
	v_mul_f32_e32 v19, 0xbfb8aa3b, v15
	v_exp_f32_e32 v18, v18
	v_exp_f32_e32 v19, v19
	v_rcp_f32_e32 v12, v12
	v_mul_f32_e32 v5, 0xbfb8aa3b, v16
	v_exp_f32_e32 v20, v5
	v_mul_f32_e32 v5, 0xbfb8aa3b, v17
	v_pk_add_f32 v[18:19], v[18:19], 1.0 op_sel_hi:[1,0]
	v_exp_f32_e32 v21, v5
	v_pk_mul_f32 v[8:9], v[8:9], v[12:13]
	v_pk_mul_f32 v[12:13], v[134:135], s[14:15] op_sel_hi:[1,0]
	v_pk_mul_f32 v[6:7], v[10:11], v[6:7]
	v_pk_mul_f32 v[8:9], v[12:13], v[8:9]
	v_pk_add_f32 v[10:11], v[20:21], 1.0 op_sel_hi:[1,0]
	v_rcp_f32_e32 v13, v19
	v_med3_f32 v9, v9, s50, v175
	v_rcp_f32_e32 v12, v18
	v_rcp_f32_e32 v11, v11
	v_rcp_f32_e32 v10, v10
	s_nop 0
	v_pk_mul_f32 v[10:11], v[16:17], v[10:11]
	v_pk_mul_f32 v[16:17], v[130:131], s[14:15] op_sel_hi:[1,0]
	v_med3_f32 v5, v8, s50, v175
	v_pk_mul_f32 v[10:11], v[16:17], v[10:11]
	v_mov_b32_e32 v8, v163
	v_med3_f32 v10, v10, s50, v175
	v_med3_f32 v11, v11, s50, v175
	v_cvt_pk_fp8_f32 v8, v5, v9
	v_mov_b32_e32 v9, v163
	v_cvt_pk_fp8_f32 v9, v10, v11
	v_pk_mul_f32 v[12:13], v[14:15], v[12:13]
	v_pk_mul_f32 v[14:15], v[132:133], s[14:15] op_sel_hi:[1,0]
	v_med3_f32 v6, v6, s50, v175
	v_pk_mul_f32 v[12:13], v[14:15], v[12:13]
	v_med3_f32 v5, v7, s50, v175
	v_med3_f32 v12, v12, s50, v175
	v_med3_f32 v7, v13, s50, v175
	v_cvt_pk_fp8_f32 v8, v6, v5 op_sel:[0,0,1]
	v_or_b32_e32 v6, 16, v4
	v_cvt_pk_fp8_f32 v9, v12, v7 op_sel:[0,0,1]
	v_ashrrev_i32_e32 v7, 31, v6
	v_lshlrev_b64 v[6:7], 8, v[6:7]
	v_lshl_add_u64 v[6:7], s[8:9], 0, v[6:7]
	v_lshl_add_u64 v[6:7], v[6:7], 0, v[162:163]
	global_store_dwordx2 v[6:7], v[8:9], off
	v_pk_mul_f32 v[6:7], v[128:129], s[12:13] op_sel_hi:[1,0]
	v_pk_mul_f32 v[8:9], v[126:127], s[12:13] op_sel_hi:[1,0]
	v_mul_f32_e32 v10, 0xbfb8aa3b, v6
	v_mul_f32_e32 v11, 0xbfb8aa3b, v7
	v_exp_f32_e32 v10, v10
	v_exp_f32_e32 v11, v11
	v_mul_f32_e32 v5, 0xbfb8aa3b, v8
	v_exp_f32_e32 v12, v5
	v_mul_f32_e32 v5, 0xbfb8aa3b, v9
	v_pk_add_f32 v[10:11], v[10:11], 1.0 op_sel_hi:[1,0]
	v_exp_f32_e32 v13, v5
	s_nop 0
	v_pk_add_f32 v[12:13], v[12:13], 1.0 op_sel_hi:[1,0]
	v_pk_mul_f32 v[14:15], v[124:125], s[12:13] op_sel_hi:[1,0]
	v_pk_mul_f32 v[16:17], v[122:123], s[12:13] op_sel_hi:[1,0]
	v_rcp_f32_e32 v11, v11
	v_readlane_b32 s59, v252, 5
	v_rcp_f32_e32 v10, v10
	s_nop 0
	v_pk_mul_f32 v[6:7], v[6:7], v[10:11]
	v_rcp_f32_e32 v13, v13
	v_pk_mul_f32 v[10:11], v[120:121], s[14:15] op_sel_hi:[1,0]
; __device__ __forceinline__ float clamp8(float v) { return __builtin_amdgcn_fmed3f(v, -448.0f, 448.0f); }
; __device__ __forceinline__ f32x4 sig4(const f32x4 v) { f32x4 r; r[0] = sigmoidf_(v[0]); r[1] = sigmoidf_(v[1]); r[2] = sigmoidf_(v[2]); r[3] = sigmoidf_(v[3]); return r; }
; #define EPI_ROWLOOP for (int ai = 0; ai < 2; ++ai) _Pragma("unroll") for (int m = 0; m < 4; ++m)
; __device__ __forceinline__ float sigmoidf_(float x) { return 1.0f / (1.0f + __expf(-x)); }
;     __device__ __forceinline__ void operator()(const f32x4 (&acc)[2][2][4][2], const pg8::Unit& u, int wr, int wc, int fr, int fq) const {
;     ...
;         EPI_ROWLOOP { const f32x4 g0 = acc[ai][0][m][0] * GU_SC, g1 = acc[ai][0][m][1] * GU_SC;
;             f32x4 h0 = g0 * sig4(g0) * (acc[ai][1][m][0] * (GU_SC * H8_SCALE)), h1 = g1 * sig4(g1) * (acc[ai][1][m][1] * (GU_SC * H8_SCALE));
; #pragma unroll
;             for (int i = 0; i < 4; ++i) { h0[i] = clamp8(h0[i]); h1[i] = clamp8(h1[i]); }
;             *(u32x2*)(HID + (size_t)(row0 + ai * 128 + m * 16) * 256 + c0) = pack8_fp8(h0, h1); }
	v_mul_f32_e32 v18, 0xbfb8aa3b, v14
	v_mul_f32_e32 v19, 0xbfb8aa3b, v15
	v_exp_f32_e32 v18, v18
	v_exp_f32_e32 v19, v19
	v_rcp_f32_e32 v12, v12
	v_mul_f32_e32 v5, 0xbfb8aa3b, v16
	v_exp_f32_e32 v20, v5
	v_mul_f32_e32 v5, 0xbfb8aa3b, v17
	v_pk_add_f32 v[18:19], v[18:19], 1.0 op_sel_hi:[1,0]
	v_exp_f32_e32 v21, v5
	v_pk_mul_f32 v[8:9], v[8:9], v[12:13]
	v_pk_mul_f32 v[12:13], v[118:119], s[14:15] op_sel_hi:[1,0]
	v_pk_mul_f32 v[6:7], v[10:11], v[6:7]
	v_pk_mul_f32 v[8:9], v[12:13], v[8:9]
	v_pk_add_f32 v[10:11], v[20:21], 1.0 op_sel_hi:[1,0]
	v_rcp_f32_e32 v13, v19
	v_med3_f32 v9, v9, s50, v175
	v_rcp_f32_e32 v12, v18
	v_rcp_f32_e32 v11, v11
	v_rcp_f32_e32 v10, v10
	s_nop 0
	v_pk_mul_f32 v[10:11], v[16:17], v[10:11]
	v_pk_mul_f32 v[16:17], v[106:107], s[14:15] op_sel_hi:[1,0]
	v_med3_f32 v5, v8, s50, v175
	v_pk_mul_f32 v[10:11], v[16:17], v[10:11]
	v_mov_b32_e32 v8, v163
	v_med3_f32 v10, v10, s50, v175
	v_med3_f32 v11, v11, s50, v175
	v_cvt_pk_fp8_f32 v8, v5, v9
	v_mov_b32_e32 v9, v163
	v_cvt_pk_fp8_f32 v9, v10, v11
	v_pk_mul_f32 v[12:13], v[14:15], v[12:13]
	v_pk_mul_f32 v[14:15], v[108:109], s[14:15] op_sel_hi:[1,0]
	v_med3_f32 v6, v6, s50, v175
	v_pk_mul_f32 v[12:13], v[14:15], v[12:13]
	v_med3_f32 v5, v7, s50, v175
	v_med3_f32 v12, v12, s50, v175
	v_med3_f32 v7, v13, s50, v175
	v_cvt_pk_fp8_f32 v8, v6, v5 op_sel:[0,0,1]
	v_or_b32_e32 v6, 32, v4
	v_cvt_pk_fp8_f32 v9, v12, v7 op_sel:[0,0,1]
	v_ashrrev_i32_e32 v7, 31, v6
	v_lshlrev_b64 v[6:7], 8, v[6:7]
	v_lshl_add_u64 v[6:7], s[8:9], 0, v[6:7]
	v_lshl_add_u64 v[6:7], v[6:7], 0, v[162:163]
	global_store_dwordx2 v[6:7], v[8:9], off
	v_pk_mul_f32 v[6:7], v[116:117], s[12:13] op_sel_hi:[1,0]
	v_pk_mul_f32 v[8:9], v[114:115], s[12:13] op_sel_hi:[1,0]
	v_mul_f32_e32 v10, 0xbfb8aa3b, v6
	v_mul_f32_e32 v11, 0xbfb8aa3b, v7
	v_exp_f32_e32 v10, v10
	v_exp_f32_e32 v11, v11
	v_mul_f32_e32 v5, 0xbfb8aa3b, v8
	v_exp_f32_e32 v12, v5
	v_mul_f32_e32 v5, 0xbfb8aa3b, v9
	v_pk_add_f32 v[10:11], v[10:11], 1.0 op_sel_hi:[1,0]
	v_exp_f32_e32 v13, v5
	s_nop 0
	v_pk_add_f32 v[12:13], v[12:13], 1.0 op_sel_hi:[1,0]
	v_pk_mul_f32 v[14:15], v[112:113], s[12:13] op_sel_hi:[1,0]
	v_pk_mul_f32 v[16:17], v[110:111], s[12:13] op_sel_hi:[1,0]
	v_rcp_f32_e32 v11, v11
	v_or_b32_e32 v4, 48, v4
	v_rcp_f32_e32 v10, v10
	s_nop 0
	v_pk_mul_f32 v[6:7], v[6:7], v[10:11]
	v_rcp_f32_e32 v13, v13
	v_pk_mul_f32 v[10:11], v[104:105], s[14:15] op_sel_hi:[1,0]
	v_mul_f32_e32 v18, 0xbfb8aa3b, v14
	v_mul_f32_e32 v19, 0xbfb8aa3b, v15
	v_exp_f32_e32 v18, v18
	v_exp_f32_e32 v19, v19
	v_rcp_f32_e32 v12, v12
	v_mul_f32_e32 v5, 0xbfb8aa3b, v16
	v_exp_f32_e32 v20, v5
	v_mul_f32_e32 v5, 0xbfb8aa3b, v17
	v_pk_add_f32 v[18:19], v[18:19], 1.0 op_sel_hi:[1,0]
	v_exp_f32_e32 v21, v5
	v_pk_mul_f32 v[8:9], v[8:9], v[12:13]
	v_pk_mul_f32 v[12:13], v[102:103], s[14:15] op_sel_hi:[1,0]
	v_pk_mul_f32 v[6:7], v[10:11], v[6:7]
	v_pk_mul_f32 v[8:9], v[12:13], v[8:9]
	v_pk_add_f32 v[10:11], v[20:21], 1.0 op_sel_hi:[1,0]
	v_rcp_f32_e32 v13, v19
	v_med3_f32 v9, v9, s50, v175
	v_rcp_f32_e32 v12, v18
	v_rcp_f32_e32 v11, v11
	v_rcp_f32_e32 v10, v10
	s_nop 0
	v_pk_mul_f32 v[10:11], v[16:17], v[10:11]
	v_pk_mul_f32 v[16:17], v[98:99], s[14:15] op_sel_hi:[1,0]
	v_med3_f32 v5, v8, s50, v175
	v_pk_mul_f32 v[10:11], v[16:17], v[10:11]
	v_mov_b32_e32 v8, v163
	v_med3_f32 v10, v10, s50, v175
	v_med3_f32 v11, v11, s50, v175
	v_cvt_pk_fp8_f32 v8, v5, v9
	v_mov_b32_e32 v9, v163
	v_cvt_pk_fp8_f32 v9, v10, v11
	v_pk_mul_f32 v[12:13], v[14:15], v[12:13]
	v_pk_mul_f32 v[14:15], v[100:101], s[14:15] op_sel_hi:[1,0]
	v_med3_f32 v6, v6, s50, v175
	v_pk_mul_f32 v[12:13], v[14:15], v[12:13]
	v_med3_f32 v5, v7, s50, v175
	v_med3_f32 v12, v12, s50, v175
	v_med3_f32 v7, v13, s50, v175
	v_cvt_pk_fp8_f32 v8, v6, v5 op_sel:[0,0,1]
	v_cvt_pk_fp8_f32 v9, v12, v7 op_sel:[0,0,1]
	v_ashrrev_i32_e32 v5, 31, v4
	v_lshlrev_b64 v[4:5], 8, v[4:5]
	v_lshl_add_u64 v[4:5], s[8:9], 0, v[4:5]
	v_lshl_add_u64 v[4:5], v[4:5], 0, v[162:163]
	global_store_dwordx2 v[4:5], v[8:9], off
	v_pk_mul_f32 v[4:5], v[96:97], s[12:13] op_sel_hi:[1,0]
	v_pk_mul_f32 v[6:7], v[94:95], s[12:13] op_sel_hi:[1,0]
	v_mul_f32_e32 v8, 0xbfb8aa3b, v4
	v_mul_f32_e32 v9, 0xbfb8aa3b, v5
	v_exp_f32_e32 v8, v8
	v_exp_f32_e32 v9, v9
	v_mul_f32_e32 v10, 0xbfb8aa3b, v6
	v_mul_f32_e32 v11, 0xbfb8aa3b, v7
	v_exp_f32_e32 v10, v10
	v_pk_add_f32 v[8:9], v[8:9], 1.0 op_sel_hi:[1,0]
	v_exp_f32_e32 v11, v11
	s_nop 0
	v_pk_add_f32 v[10:11], v[10:11], 1.0 op_sel_hi:[1,0]
	v_pk_mul_f32 v[12:13], v[92:93], s[12:13] op_sel_hi:[1,0]
	v_pk_mul_f32 v[14:15], v[90:91], s[12:13] op_sel_hi:[1,0]
	v_rcp_f32_e32 v9, v9
	v_rcp_f32_e32 v8, v8
	s_nop 0
	v_pk_mul_f32 v[4:5], v[4:5], v[8:9]
	v_rcp_f32_e32 v11, v11
	v_pk_mul_f32 v[8:9], v[88:89], s[14:15] op_sel_hi:[1,0]
	v_rcp_f32_e32 v10, v10
	v_mul_f32_e32 v16, 0xbfb8aa3b, v12
	v_mul_f32_e32 v17, 0xbfb8aa3b, v13
	v_exp_f32_e32 v16, v16
	v_exp_f32_e32 v17, v17
	v_mul_f32_e32 v18, 0xbfb8aa3b, v14
	v_mul_f32_e32 v19, 0xbfb8aa3b, v15
	v_pk_mul_f32 v[6:7], v[6:7], v[10:11]
	v_pk_add_f32 v[16:17], v[16:17], 1.0 op_sel_hi:[1,0]
	v_pk_mul_f32 v[10:11], v[86:87], s[14:15] op_sel_hi:[1,0]
	v_exp_f32_e32 v18, v18
	v_exp_f32_e32 v19, v19
	v_pk_mul_f32 v[6:7], v[10:11], v[6:7]
	v_pk_mul_f32 v[4:5], v[8:9], v[4:5]
	v_pk_add_f32 v[8:9], v[18:19], 1.0 op_sel_hi:[1,0]
	v_rcp_f32_e32 v11, v17
	v_rcp_f32_e32 v10, v16
	s_nop 0
	v_pk_mul_f32 v[10:11], v[12:13], v[10:11]
	v_rcp_f32_e32 v9, v9
	v_pk_mul_f32 v[12:13], v[76:77], s[14:15] op_sel_hi:[1,0]
	v_rcp_f32_e32 v8, v8
	s_nop 0
	v_pk_mul_f32 v[8:9], v[14:15], v[8:9]
	v_pk_mul_f32 v[14:15], v[74:75], s[14:15] op_sel_hi:[1,0]
	v_pk_mul_f32 v[10:11], v[12:13], v[10:11]
; __device__ __forceinline__ float clamp8(float v) { return __builtin_amdgcn_fmed3f(v, -448.0f, 448.0f); }
; __device__ __forceinline__ f32x4 sig4(const f32x4 v) { f32x4 r; r[0] = sigmoidf_(v[0]); r[1] = sigmoidf_(v[1]); r[2] = sigmoidf_(v[2]); r[3] = sigmoidf_(v[3]); return r; }
; #define EPI_ROWLOOP for (int ai = 0; ai < 2; ++ai) _Pragma("unroll") for (int m = 0; m < 4; ++m)
; __device__ __forceinline__ float sigmoidf_(float x) { return 1.0f / (1.0f + __expf(-x)); }
;     __device__ __forceinline__ void operator()(const f32x4 (&acc)[2][2][4][2], const pg8::Unit& u, int wr, int wc, int fr, int fq) const {
;     ...
;         EPI_ROWLOOP { const f32x4 g0 = acc[ai][0][m][0] * GU_SC, g1 = acc[ai][0][m][1] * GU_SC;
;             f32x4 h0 = g0 * sig4(g0) * (acc[ai][1][m][0] * (GU_SC * H8_SCALE)), h1 = g1 * sig4(g1) * (acc[ai][1][m][1] * (GU_SC * H8_SCALE));
; #pragma unroll
;             for (int i = 0; i < 4; ++i) { h0[i] = clamp8(h0[i]); h1[i] = clamp8(h1[i]); }
;             *(u32x2*)(HID + (size_t)(row0 + ai * 128 + m * 16) * 256 + c0) = pack8_fp8(h0, h1); }
	v_pk_mul_f32 v[8:9], v[14:15], v[8:9]
	v_med3_f32 v12, v6, s50, v175
	v_med3_f32 v7, v7, s50, v175
	v_mov_b32_e32 v6, v163
	v_med3_f32 v8, v8, s50, v175
	v_med3_f32 v9, v9, s50, v175
	v_cvt_pk_fp8_f32 v6, v12, v7
	v_mov_b32_e32 v7, v163
	v_cvt_pk_fp8_f32 v7, v8, v9
	v_med3_f32 v4, v4, s50, v175
	v_med3_f32 v5, v5, s50, v175
	v_med3_f32 v10, v10, s50, v175
	v_med3_f32 v8, v11, s50, v175
	v_cvt_pk_fp8_f32 v6, v4, v5 op_sel:[0,0,1]
	v_pk_mul_f32 v[4:5], v[84:85], s[12:13] op_sel_hi:[1,0]
	v_cvt_pk_fp8_f32 v7, v10, v8 op_sel:[0,0,1]
	v_mul_f32_e32 v10, 0xbfb8aa3b, v4
	v_mul_f32_e32 v11, 0xbfb8aa3b, v5
	v_exp_f32_e32 v10, v10
	v_exp_f32_e32 v11, v11
	v_pk_mul_f32 v[8:9], v[82:83], s[12:13] op_sel_hi:[1,0]
	v_pk_mul_f32 v[14:15], v[80:81], s[12:13] op_sel_hi:[1,0]
	v_mul_f32_e32 v12, 0xbfb8aa3b, v8
	v_pk_add_f32 v[10:11], v[10:11], 1.0 op_sel_hi:[1,0]
	v_mul_f32_e32 v13, 0xbfb8aa3b, v9
	v_exp_f32_e32 v12, v12
	v_exp_f32_e32 v13, v13
	v_pk_mul_f32 v[16:17], v[78:79], s[12:13] op_sel_hi:[1,0]
	v_rcp_f32_e32 v11, v11
	v_pk_add_f32 v[12:13], v[12:13], 1.0 op_sel_hi:[1,0]
	v_rcp_f32_e32 v10, v10
	s_nop 0
	v_pk_mul_f32 v[4:5], v[4:5], v[10:11]
	v_rcp_f32_e32 v13, v13
	v_pk_mul_f32 v[10:11], v[72:73], s[14:15] op_sel_hi:[1,0]
	v_rcp_f32_e32 v12, v12
	v_mul_f32_e32 v18, 0xbfb8aa3b, v14
	v_mul_f32_e32 v19, 0xbfb8aa3b, v15
	v_exp_f32_e32 v18, v18
	v_exp_f32_e32 v19, v19
	v_mul_f32_e32 v20, 0xbfb8aa3b, v16
	v_mul_f32_e32 v21, 0xbfb8aa3b, v17
	v_pk_mul_f32 v[8:9], v[8:9], v[12:13]
	v_pk_add_f32 v[18:19], v[18:19], 1.0 op_sel_hi:[1,0]
	v_pk_mul_f32 v[12:13], v[70:71], s[14:15] op_sel_hi:[1,0]
	v_exp_f32_e32 v20, v20
	v_exp_f32_e32 v21, v21
	v_pk_mul_f32 v[8:9], v[12:13], v[8:9]
	v_pk_mul_f32 v[4:5], v[10:11], v[4:5]
	v_pk_add_f32 v[10:11], v[20:21], 1.0 op_sel_hi:[1,0]
	v_rcp_f32_e32 v13, v19
	v_rcp_f32_e32 v12, v18
	s_nop 0
	v_pk_mul_f32 v[12:13], v[14:15], v[12:13]
	v_rcp_f32_e32 v11, v11
	v_pk_mul_f32 v[14:15], v[64:65], s[14:15] op_sel_hi:[1,0]
	v_rcp_f32_e32 v10, v10
	s_nop 0
	v_pk_mul_f32 v[10:11], v[16:17], v[10:11]
	v_pk_mul_f32 v[16:17], v[62:63], s[14:15] op_sel_hi:[1,0]
	v_pk_mul_f32 v[12:13], v[14:15], v[12:13]
	v_pk_mul_f32 v[10:11], v[16:17], v[10:11]
	v_med3_f32 v14, v8, s50, v175
	v_med3_f32 v9, v9, s50, v175
	v_mov_b32_e32 v8, v163
	v_med3_f32 v10, v10, s50, v175
	v_med3_f32 v11, v11, s50, v175
	v_cvt_pk_fp8_f32 v8, v14, v9
	v_mov_b32_e32 v9, v163
	v_cvt_pk_fp8_f32 v9, v10, v11
	v_med3_f32 v4, v4, s50, v175
	v_med3_f32 v12, v12, s50, v175
	v_med3_f32 v5, v5, s50, v175
	v_med3_f32 v10, v13, s50, v175
	v_cvt_pk_fp8_f32 v8, v4, v5 op_sel:[0,0,1]
	v_cvt_pk_fp8_f32 v9, v12, v10 op_sel:[0,0,1]
	v_add_co_u32_e32 v4, vcc, s51, v2
	v_pk_mul_f32 v[12:13], v[60:61], s[12:13] op_sel_hi:[1,0]
	s_nop 0
	v_addc_co_u32_e32 v5, vcc, 0, v3, vcc
	global_store_dwordx2 v[4:5], v[6:7], off offset:-4096
	global_store_dwordx2 v[4:5], v[8:9], off
	v_pk_mul_f32 v[4:5], v[68:69], s[12:13] op_sel_hi:[1,0]
	v_pk_mul_f32 v[6:7], v[66:67], s[12:13] op_sel_hi:[1,0]
	v_mul_f32_e32 v8, 0xbfb8aa3b, v4
	v_mul_f32_e32 v9, 0xbfb8aa3b, v5
	v_exp_f32_e32 v8, v8
	v_exp_f32_e32 v9, v9
	v_mul_f32_e32 v10, 0xbfb8aa3b, v6
	v_mul_f32_e32 v11, 0xbfb8aa3b, v7
	v_exp_f32_e32 v10, v10
	v_pk_add_f32 v[8:9], v[8:9], 1.0 op_sel_hi:[1,0]
	v_exp_f32_e32 v11, v11
	s_nop 0
	v_pk_add_f32 v[10:11], v[10:11], 1.0 op_sel_hi:[1,0]
	v_pk_mul_f32 v[14:15], v[58:59], s[12:13] op_sel_hi:[1,0]
	v_rcp_f32_e32 v9, v9
	v_rcp_f32_e32 v8, v8
	s_nop 0
	v_pk_mul_f32 v[4:5], v[4:5], v[8:9]
	v_rcp_f32_e32 v11, v11
	v_pk_mul_f32 v[8:9], v[56:57], s[14:15] op_sel_hi:[1,0]
	v_rcp_f32_e32 v10, v10
	v_mul_f32_e32 v16, 0xbfb8aa3b, v12
	v_mul_f32_e32 v17, 0xbfb8aa3b, v13
	v_exp_f32_e32 v16, v16
	v_exp_f32_e32 v17, v17
	v_mul_f32_e32 v18, 0xbfb8aa3b, v14
; __device__ __forceinline__ float clamp8(float v) { return __builtin_amdgcn_fmed3f(v, -448.0f, 448.0f); }
; #define PG8_BAR __builtin_amdgcn_s_barrier()
; #define PG8_ZERO_W() do { if constexpr (F8) { _Pragma("unroll") for (int _a = 0; _a < 2; ++_a) _Pragma("unroll") for (int _b = 0; _b < 2; ++_b) _Pragma("unroll") for (int _m = 0; _m < 2; ++_m) _Pragma("unroll") for (int _e = 0; _e < 16; ++_e) accw[_a][_b][_m][_e] = 0.f; } } while (0)
; __device__ __forceinline__ f32x4 sig4(const f32x4 v) { f32x4 r; r[0] = sigmoidf_(v[0]); r[1] = sigmoidf_(v[1]); r[2] = sigmoidf_(v[2]); r[3] = sigmoidf_(v[3]); return r; }
; #define EPI_ROWLOOP for (int ai = 0; ai < 2; ++ai) _Pragma("unroll") for (int m = 0; m < 4; ++m)
;     ...
;         E(acc, cur, wr, wc, fr, fq);
;         PG8_ZERO_W();
;         if (!has_next) break;
; #pragma unroll
;         for (int a = 0; a < 2; ++a)
; #pragma unroll
;             for (int b = 0; b < 2; ++b)
; #pragma unroll
;                 for (int m = 0; m < 4; ++m)
; #pragma unroll
;                     for (int n = 0; n < 2; ++n) acc[a][b][m][n] = (f32x4){0.f, 0.f, 0.f, 0.f};
;         cur = nxt; cB = nB; ++ui;
; #pragma unroll
;         for (int h = 0; h < 2; ++h) { uC[h] = uN[h];
; #pragma unroll
;             for (int i = 0; i < 2; ++i) aoC[h][i] = aoN[h][i]; }
;         if constexpr (ALIGN_EPI) { if (wr == 1) PG8_BAR; }
;     __device__ __forceinline__ void operator()(const f32x4 (&acc)[2][2][4][2], const pg8::Unit& u, int wr, int wc, int fr, int fq) const {
;     ...
;         EPI_ROWLOOP { const f32x4 g0 = acc[ai][0][m][0] * GU_SC, g1 = acc[ai][0][m][1] * GU_SC;
;             f32x4 h0 = g0 * sig4(g0) * (acc[ai][1][m][0] * (GU_SC * H8_SCALE)), h1 = g1 * sig4(g1) * (acc[ai][1][m][1] * (GU_SC * H8_SCALE));
; #pragma unroll
;             for (int i = 0; i < 4; ++i) { h0[i] = clamp8(h0[i]); h1[i] = clamp8(h1[i]); }
;             *(u32x2*)(HID + (size_t)(row0 + ai * 128 + m * 16) * 256 + c0) = pack8_fp8(h0, h1); }
	v_mul_f32_e32 v19, 0xbfb8aa3b, v15
	v_pk_mul_f32 v[6:7], v[6:7], v[10:11]
	v_pk_add_f32 v[16:17], v[16:17], 1.0 op_sel_hi:[1,0]
	v_pk_mul_f32 v[10:11], v[54:55], s[14:15] op_sel_hi:[1,0]
	v_exp_f32_e32 v18, v18
	v_exp_f32_e32 v19, v19
	v_pk_mul_f32 v[6:7], v[10:11], v[6:7]
	v_pk_mul_f32 v[4:5], v[8:9], v[4:5]
	v_pk_add_f32 v[8:9], v[18:19], 1.0 op_sel_hi:[1,0]
	v_rcp_f32_e32 v11, v17
	v_rcp_f32_e32 v10, v16
	s_nop 0
	v_pk_mul_f32 v[10:11], v[12:13], v[10:11]
	v_rcp_f32_e32 v9, v9
	v_pk_mul_f32 v[12:13], v[44:45], s[14:15] op_sel_hi:[1,0]
	v_rcp_f32_e32 v8, v8
	s_nop 0
	v_pk_mul_f32 v[8:9], v[14:15], v[8:9]
	v_pk_mul_f32 v[14:15], v[42:43], s[14:15] op_sel_hi:[1,0]
	v_pk_mul_f32 v[10:11], v[12:13], v[10:11]
	v_pk_mul_f32 v[8:9], v[14:15], v[8:9]
	v_med3_f32 v12, v6, s50, v175
	v_med3_f32 v7, v7, s50, v175
	v_mov_b32_e32 v6, v163
	v_med3_f32 v8, v8, s50, v175
	v_med3_f32 v9, v9, s50, v175
	v_cvt_pk_fp8_f32 v6, v12, v7
	v_mov_b32_e32 v7, v163
	v_cvt_pk_fp8_f32 v7, v8, v9
	v_med3_f32 v4, v4, s50, v175
	v_med3_f32 v10, v10, s50, v175
	v_med3_f32 v5, v5, s50, v175
	v_med3_f32 v8, v11, s50, v175
	v_cvt_pk_fp8_f32 v6, v4, v5 op_sel:[0,0,1]
	v_cvt_pk_fp8_f32 v7, v10, v8 op_sel:[0,0,1]
	v_add_co_u32_e32 v4, vcc, s47, v2
	v_pk_mul_f32 v[12:13], v[48:49], s[12:13] op_sel_hi:[1,0]
	s_nop 0
	v_addc_co_u32_e32 v5, vcc, 0, v3, vcc
	global_store_dwordx2 v[4:5], v[6:7], off
	v_pk_mul_f32 v[4:5], v[52:53], s[12:13] op_sel_hi:[1,0]
	v_pk_mul_f32 v[6:7], v[50:51], s[12:13] op_sel_hi:[1,0]
	v_mul_f32_e32 v8, 0xbfb8aa3b, v4
	v_mul_f32_e32 v9, 0xbfb8aa3b, v5
	v_exp_f32_e32 v8, v8
	v_exp_f32_e32 v9, v9
	v_mul_f32_e32 v10, 0xbfb8aa3b, v6
	v_mul_f32_e32 v11, 0xbfb8aa3b, v7
	v_exp_f32_e32 v10, v10
	v_pk_add_f32 v[8:9], v[8:9], 1.0 op_sel_hi:[1,0]
	v_exp_f32_e32 v11, v11
	s_nop 0
	v_pk_add_f32 v[10:11], v[10:11], 1.0 op_sel_hi:[1,0]
	v_pk_mul_f32 v[14:15], v[46:47], s[12:13] op_sel_hi:[1,0]
	v_rcp_f32_e32 v9, v9
	v_rcp_f32_e32 v8, v8
	s_nop 0
	v_pk_mul_f32 v[4:5], v[4:5], v[8:9]
	v_rcp_f32_e32 v11, v11
	v_pk_mul_f32 v[8:9], v[40:41], s[14:15] op_sel_hi:[1,0]
	v_rcp_f32_e32 v10, v10
	v_mul_f32_e32 v16, 0xbfb8aa3b, v12
	v_mul_f32_e32 v17, 0xbfb8aa3b, v13
	v_exp_f32_e32 v16, v16
	v_exp_f32_e32 v17, v17
	v_mul_f32_e32 v18, 0xbfb8aa3b, v14
	v_mul_f32_e32 v19, 0xbfb8aa3b, v15
	v_pk_mul_f32 v[6:7], v[6:7], v[10:11]
	v_pk_add_f32 v[16:17], v[16:17], 1.0 op_sel_hi:[1,0]
	v_pk_mul_f32 v[10:11], v[38:39], s[14:15] op_sel_hi:[1,0]
	v_exp_f32_e32 v18, v18
	v_exp_f32_e32 v19, v19
	v_pk_mul_f32 v[6:7], v[10:11], v[6:7]
	v_pk_mul_f32 v[4:5], v[8:9], v[4:5]
	v_pk_add_f32 v[8:9], v[18:19], 1.0 op_sel_hi:[1,0]
	v_rcp_f32_e32 v11, v17
	v_rcp_f32_e32 v10, v16
	s_nop 0
	v_pk_mul_f32 v[10:11], v[12:13], v[10:11]
	v_rcp_f32_e32 v9, v9
	v_pk_mul_f32 v[12:13], v[36:37], s[14:15] op_sel_hi:[1,0]
	v_rcp_f32_e32 v8, v8
	s_nop 0
	v_pk_mul_f32 v[8:9], v[14:15], v[8:9]
	v_pk_mul_f32 v[14:15], v[34:35], s[14:15] op_sel_hi:[1,0]
	v_pk_mul_f32 v[10:11], v[12:13], v[10:11]
	v_pk_mul_f32 v[8:9], v[14:15], v[8:9]
	v_med3_f32 v12, v6, s50, v175
	v_med3_f32 v7, v7, s50, v175
	v_mov_b32_e32 v6, v163
	v_med3_f32 v8, v8, s50, v175
	v_med3_f32 v9, v9, s50, v175
	v_cvt_pk_fp8_f32 v6, v12, v7
	v_mov_b32_e32 v7, v163
	v_cvt_pk_fp8_f32 v7, v8, v9
	v_med3_f32 v4, v4, s50, v175
	v_med3_f32 v10, v10, s50, v175
	v_med3_f32 v5, v5, s50, v175
	v_med3_f32 v8, v11, s50, v175
	v_cvt_pk_fp8_f32 v6, v4, v5 op_sel:[0,0,1]
	v_cvt_pk_fp8_f32 v7, v10, v8 op_sel:[0,0,1]
	v_add_co_u32_e32 v2, vcc, 0xb000, v2
	s_nop 1
	v_addc_co_u32_e32 v3, vcc, 0, v3, vcc
	s_and_b64 vcc, exec, s[4:5]
	s_mov_b64 s[4:5], -1
	global_store_dwordx2 v[2:3], v[6:7], off
	s_cbranch_vccnz .LBB0_2694
	s_andn2_b64 vcc, exec, s[6:7]
	s_cbranch_vccnz .LBB0_2693
	s_barrier
	s_branch .LBB0_2693
